# K2: out-degree overflow loads issued at loop start (atomics at tail); iso_g stores merged into tile epilogue
# baseline (speedup 1.0000x reference)
.LBB1_45:
	s_or_b64 exec, exec, s[0:1]
	v_mbcnt_lo_u32_b32 v190, -1, 0
	v_mbcnt_hi_u32_b32 v190, -1, v190
	v_mad_u32_u24 v191, v190, 5, v164
	s_movk_i32 s44, 0x100
	v_cmp_gt_u32_e32 vcc, s44, v191
	s_mov_b64 exec, vcc
	v_lshlrev_b32_e32 v191, 2, v191
	v_add_u32_e32 v198, 0x18b40, v191
	v_add_u32_e32 v199, 0x18fc0, v191
	ds_read_b32 v196, v198
	ds_read_b32 v197, v199
	s_waitcnt lgkmcnt(0)
	v_cmp_lt_u32_e32 vcc, 64, v196
	s_mov_b64 s[42:43], vcc
	s_mov_b64 exec, -1
	v_or_b32_e32 v198, 64, v190
	v_lshlrev_b32_e32 v199, 1, v190
	s_mov_b64 s[46:47], 0
	s_mov_b64 s[48:49], 0
	s_mov_b64 s[50:51], 0
	s_mov_b64 s[52:53], 0
	s_cmp_eq_u64 s[42:43], 0
	s_cbranch_scc1 .Lk2e_done
	s_ff1_i32_b64 s44, s[42:43]
	v_readlane_b32 s45, v196, s44
	v_readlane_b32 s54, v197, s44
	s_bitset0_b64 s[42:43], s44
	s_nop 0
	v_cmp_gt_u32_e64 s[46:47], s45, v198
	s_add_i32 s54, s54, 64
	s_lshl_b32 s54, s54, 1
	s_add_u32 s56, s26, s54
	s_addc_u32 s57, s27, 0
	s_mov_b64 exec, s[46:47]
	global_load_ushort v192, v199, s[56:57]
	s_mov_b64 exec, -1
	s_cmp_eq_u64 s[42:43], 0
	s_cbranch_scc1 .Lk2e_done
	s_ff1_i32_b64 s44, s[42:43]
	v_readlane_b32 s45, v196, s44
	v_readlane_b32 s54, v197, s44
	s_bitset0_b64 s[42:43], s44
	s_nop 0
	v_cmp_gt_u32_e64 s[48:49], s45, v198
	s_add_i32 s54, s54, 64
	s_lshl_b32 s54, s54, 1
	s_add_u32 s58, s26, s54
	s_addc_u32 s59, s27, 0
	s_mov_b64 exec, s[48:49]
	global_load_ushort v193, v199, s[58:59]
	s_mov_b64 exec, -1
	s_cmp_eq_u64 s[42:43], 0
	s_cbranch_scc1 .Lk2e_done
	s_ff1_i32_b64 s44, s[42:43]
	v_readlane_b32 s45, v196, s44
	v_readlane_b32 s54, v197, s44
	s_bitset0_b64 s[42:43], s44
	s_nop 0
	v_cmp_gt_u32_e64 s[50:51], s45, v198
	s_add_i32 s54, s54, 64
	s_lshl_b32 s54, s54, 1
	s_add_u32 s60, s26, s54
	s_addc_u32 s61, s27, 0
	s_mov_b64 exec, s[50:51]
	global_load_ushort v194, v199, s[60:61]
	s_mov_b64 exec, -1
	s_cmp_eq_u64 s[42:43], 0
	s_cbranch_scc1 .Lk2e_done
	s_ff1_i32_b64 s44, s[42:43]
	v_readlane_b32 s45, v196, s44
	v_readlane_b32 s54, v197, s44
	s_bitset0_b64 s[42:43], s44
	s_nop 0
	v_cmp_gt_u32_e64 s[52:53], s45, v198
	s_add_i32 s54, s54, 64
	s_lshl_b32 s54, s54, 1
	s_add_u32 s62, s26, s54
	s_addc_u32 s63, s27, 0
	s_mov_b64 exec, s[52:53]
	global_load_ushort v195, v199, s[62:63]
	s_mov_b64 exec, -1
.Lk2e_done:
	v_lshlrev_b32_e32 v130, 2, v130
	v_mov_b32_e32 v131, 0
	v_lshlrev_b32_e32 v134, 2, v164
	v_lshl_add_u64 v[162:163], s[8:9], 0, v[130:131]
	v_mov_b32_e32 v183, v1
	v_or_b32_e32 v169, 0x18fc0, v134
	v_add_u32_e32 v130, 0x18fd4, v134
	v_add_u32_e32 v135, 0x18b68, v134
	v_add_u32_e32 v136, 0x18ffc, v134
	v_add_u32_e32 v137, 0x18b7c, v134
	v_or_b32_e32 v170, 0x18b40, v134
	v_add_u32_e32 v132, 0x18b54, v134
	v_add_u32_e32 v133, 0x18fe8, v134
	ds_read_b32 v138, v169
	ds_read_b32 v139, v170
	ds_read_b32 v140, v130
	ds_read_b32 v141, v132
	ds_read_b32 v142, v133
	ds_read_b32 v135, v135
	ds_read_b32 v136, v136
	ds_read_b32 v137, v137
	s_waitcnt lgkmcnt(7)
	v_add_u32_e32 v130, v138, v1
	s_waitcnt lgkmcnt(6)
	v_cmp_lt_u32_e64 s[18:19], v1, v139
	s_waitcnt lgkmcnt(4)
	v_cmp_lt_u32_e32 vcc, v1, v141
	s_waitcnt lgkmcnt(2)
	v_cmp_lt_u32_e64 s[8:9], v1, v135
	v_cndmask_b32_e64 v130, 0, v130, s[18:19]
	v_lshl_add_u64 v[132:133], v[130:131], 1, s[26:27]
	v_add_u32_e32 v130, v140, v1
	v_cndmask_b32_e32 v130, 0, v130, vcc
	global_load_ushort v181, v[132:133], off
	v_lshl_add_u64 v[132:133], v[130:131], 1, s[26:27]
	v_add_u32_e32 v130, v142, v1
	v_cndmask_b32_e64 v130, 0, v130, s[8:9]
	global_load_ushort v178, v[132:133], off
	v_lshl_add_u64 v[132:133], v[130:131], 1, s[26:27]
	s_waitcnt lgkmcnt(1)
	v_add_u32_e32 v130, v136, v1
	s_waitcnt lgkmcnt(0)
	v_cmp_lt_u32_e64 s[4:5], v1, v137
	global_load_ushort v176, v[132:133], off
	v_add_u32_e32 v135, 0x18ba4, v134
	v_cndmask_b32_e64 v130, 0, v130, s[4:5]
	v_lshl_add_u64 v[132:133], v[130:131], 1, s[26:27]
	global_load_ushort v172, v[132:133], off
	v_add_u32_e32 v130, 0x19010, v134
	v_add_u32_e32 v132, 0x18b90, v134
	v_add_u32_e32 v136, 0x19038, v134
	v_add_u32_e32 v137, 0x18bb8, v134
	v_add_u32_e32 v138, 0x1904c, v134
	v_add_u32_e32 v139, 0x18bcc, v134
	v_add_u32_e32 v133, 0x19024, v134
	ds_read_b32 v130, v130
	ds_read_b32 v132, v132
	ds_read_b32 v140, v133
	ds_read_b32 v135, v135
	ds_read_b32 v136, v136
	ds_read_b32 v137, v137
	ds_read_b32 v138, v138
	ds_read_b32 v139, v139
	s_waitcnt lgkmcnt(7)
	v_add_u32_e32 v130, v130, v1
	s_waitcnt lgkmcnt(6)
	v_cmp_lt_u32_e64 s[20:21], v1, v132
	s_waitcnt lgkmcnt(4)
	v_cmp_lt_u32_e64 s[16:17], v1, v135
	s_waitcnt lgkmcnt(2)
	v_cmp_lt_u32_e64 s[10:11], v1, v137
	v_cndmask_b32_e64 v130, 0, v130, s[20:21]
	v_lshl_add_u64 v[132:133], v[130:131], 1, s[26:27]
	v_add_u32_e32 v130, v140, v1
	v_cndmask_b32_e64 v130, 0, v130, s[16:17]
	global_load_ushort v182, v[132:133], off
	v_lshl_add_u64 v[132:133], v[130:131], 1, s[26:27]
	v_add_u32_e32 v130, v136, v1
	v_cndmask_b32_e64 v130, 0, v130, s[10:11]
	global_load_ushort v179, v[132:133], off
	v_lshl_add_u64 v[132:133], v[130:131], 1, s[26:27]
	s_waitcnt lgkmcnt(1)
	v_add_u32_e32 v130, v138, v1
	s_waitcnt lgkmcnt(0)
	v_cmp_lt_u32_e64 s[6:7], v1, v139
	global_load_ushort v177, v[132:133], off
	v_add_u32_e32 v135, 0x18bf4, v134
	v_cndmask_b32_e64 v130, 0, v130, s[6:7]
	v_lshl_add_u64 v[132:133], v[130:131], 1, s[26:27]
	global_load_ushort v173, v[132:133], off
	v_or_b32_e32 v130, 0x19060, v134
	v_or_b32_e32 v132, 0x18be0, v134
	v_add_u32_e32 v133, 0x19074, v134
	v_add_u32_e32 v136, 0x19088, v134
	v_add_u32_e32 v134, 0x18c08, v134
	ds_read_b32 v130, v130
	ds_read_b32 v132, v132
	ds_read_b32 v137, v133
	ds_read_b32 v135, v135
	ds_read_b32 v136, v136
	ds_read_b32 v134, v134
	s_waitcnt lgkmcnt(5)
	v_add_u32_e32 v130, v130, v1
	s_waitcnt lgkmcnt(4)
	v_cmp_lt_u32_e64 s[14:15], v1, v132
	s_waitcnt lgkmcnt(2)
	v_cmp_lt_u32_e64 s[12:13], v1, v135
	s_movk_i32 s22, 0x4100
	v_cndmask_b32_e64 v130, 0, v130, s[14:15]
	v_lshl_add_u64 v[132:133], v[130:131], 1, s[26:27]
	v_add_u32_e32 v130, v137, v1
	v_cndmask_b32_e64 v130, 0, v130, s[12:13]
	global_load_ushort v180, v[132:133], off
	v_lshl_add_u64 v[132:133], v[130:131], 1, s[26:27]
	s_waitcnt lgkmcnt(1)
	v_add_u32_e32 v130, v136, v1
	s_waitcnt lgkmcnt(0)
	v_cmp_lt_u32_e64 s[0:1], v1, v134
	global_load_ushort v175, v[132:133], off
	v_lshrrev_b32_e32 v167, 4, v1
	v_cndmask_b32_e64 v130, 0, v130, s[0:1]
	v_lshl_add_u64 v[130:131], v[130:131], 1, s[26:27]
	global_load_ushort v174, v[130:131], off
	v_lshlrev_b32_e32 v130, 3, v1
	v_mad_u32_u24 v171, v164, s22, v130
	v_mul_u32_u24_e32 v130, 0x410, v166
	v_mad_u32_u24 v130, v164, s22, v130
	v_lshlrev_b32_e32 v131, 8, v167
	v_add_u32_e32 v168, v130, v131
	s_add_i32 s33, s30, 0x50
	s_add_i32 s31, s30, 0x58
	s_waitcnt vmcnt(27)
	v_cvt_pk_bf16_f32 v106, v106, v107
	v_cvt_pk_bf16_f32 v107, v108, v109
	v_cvt_pk_bf16_f32 v102, v102, v103
	v_cvt_pk_bf16_f32 v103, v104, v105
	ds_write2_b64 v171, v[106:107], v[102:103] offset0:130 offset1:194
	v_cvt_pk_bf16_f32 v102, v126, v127
	v_cvt_pk_bf16_f32 v103, v128, v129
	v_cvt_pk_bf16_f32 v104, v110, v111
	v_cvt_pk_bf16_f32 v105, v112, v113
	v_add_u32_e32 v106, 32, v171
	v_cvt_pk_bf16_f32 v86, v86, v87
	v_cvt_pk_bf16_f32 v87, v88, v89
	v_cvt_pk_bf16_f32 v78, v78, v79
	v_cvt_pk_bf16_f32 v79, v80, v81
	v_add_u32_e32 v80, 0x50, v171
	v_cvt_pk_bf16_f32 v122, v122, v123
	v_cvt_pk_bf16_f32 v123, v124, v125
	v_cvt_pk_bf16_f32 v118, v118, v119
	v_cvt_pk_bf16_f32 v119, v120, v121
	ds_write2st64_b64 v106, v[102:103], v[104:105] offset0:4 offset1:5
	v_cvt_pk_bf16_f32 v98, v98, v99
	v_cvt_pk_bf16_f32 v99, v100, v101
	v_cvt_pk_bf16_f32 v100, v114, v115
	v_cvt_pk_bf16_f32 v101, v116, v117
	v_add_u32_e32 v102, 48, v171
	v_cvt_pk_bf16_f32 v94, v94, v95
	v_cvt_pk_bf16_f32 v95, v96, v97
	v_cvt_pk_bf16_f32 v90, v90, v91
	v_cvt_pk_bf16_f32 v91, v92, v93
	v_add_u32_e32 v92, 64, v171
	ds_write2st64_b64 v80, v[86:87], v[78:79] offset0:10 offset1:11
	v_cvt_pk_bf16_f32 v78, v82, v83
	v_cvt_pk_bf16_f32 v79, v84, v85
	v_cvt_pk_bf16_f32 v74, v74, v75
	v_cvt_pk_bf16_f32 v75, v76, v77
	v_add_u32_e32 v76, 0x60, v171
	v_cvt_pk_bf16_f32 v70, v70, v71
	v_cvt_pk_bf16_f32 v71, v72, v73
	v_cvt_pk_bf16_f32 v66, v66, v67
	v_cvt_pk_bf16_f32 v67, v68, v69
	v_add_u32_e32 v68, 0x70, v171
	ds_write2st64_b64 v171, v[122:123], v[118:119] offset1:1
	ds_write2st64_b64 v102, v[98:99], v[100:101] offset0:6 offset1:7
	ds_write2st64_b64 v92, v[94:95], v[90:91] offset0:8 offset1:9
	ds_write2st64_b64 v76, v[78:79], v[74:75] offset0:12 offset1:13
	ds_write2st64_b64 v68, v[70:71], v[66:67] offset0:14 offset1:15
	v_add_u32_e32 v66, s33, v165
	v_min_i32_e32 v66, 0x18698, v66
	v_ashrrev_i32_e32 v67, 31, v66
	v_lshlrev_b64 v[66:67], 11, v[66:67]
	v_lshl_add_u64 v[66:67], v[162:163], 0, v[66:67]
	s_movk_i32 s34, 0x1000
	v_add_co_u32_e64 v68, s[22:23], s34, v66
	s_movk_i32 s35, 0x2000
	s_nop 0
	v_addc_co_u32_e64 v69, s[22:23], 0, v67, s[22:23]
	v_add_co_u32_e64 v98, s[22:23], s35, v66
	s_movk_i32 s36, 0x3000
	s_nop 0
	v_addc_co_u32_e64 v99, s[22:23], 0, v67, s[22:23]
	global_load_dwordx4 v[146:149], v[66:67], off nt
	global_load_dwordx4 v[138:141], v[66:67], off offset:1024 nt
	global_load_dwordx4 v[126:129], v[66:67], off offset:2048 nt
	global_load_dwordx4 v[118:121], v[66:67], off offset:3072 nt
	v_add_co_u32_e64 v66, s[22:23], s36, v66
	global_load_dwordx4 v[130:133], v[68:69], off offset:1024 nt
	global_load_dwordx4 v[102:105], v[68:69], off offset:2048 nt
	global_load_dwordx4 v[94:97], v[98:99], off nt
	global_load_dwordx4 v[90:93], v[98:99], off offset:1024 nt
	global_load_dwordx4 v[86:89], v[98:99], off offset:2048 nt
	global_load_dwordx4 v[78:81], v[98:99], off offset:3072 nt
	v_addc_co_u32_e64 v67, s[22:23], 0, v67, s[22:23]
	global_load_dwordx4 v[134:137], v[68:69], off offset:3072 nt
	global_load_dwordx4 v[82:85], v[66:67], off nt
	global_load_dwordx4 v[74:77], v[66:67], off offset:1024 nt
	global_load_dwordx4 v[70:73], v[66:67], off offset:2048 nt
	global_load_dwordx4 v[158:161], v[98:99], off offset:-4096 nt
	s_nop 0
	global_load_dwordx4 v[66:69], v[66:67], off offset:3072 nt
	s_waitcnt vmcnt(27)
	v_cvt_pk_bf16_f32 v50, v50, v51
	v_cvt_pk_bf16_f32 v51, v52, v53
	v_cvt_pk_bf16_f32 v38, v38, v39
	v_cvt_pk_bf16_f32 v39, v40, v41
	v_add_u32_e32 v40, 0x90, v171
	ds_write2st64_b64 v40, v[50:51], v[38:39] offset0:18 offset1:19
	v_cvt_pk_bf16_f32 v38, v62, v63
	v_cvt_pk_bf16_f32 v39, v64, v65
	v_cvt_pk_bf16_f32 v40, v42, v43
	v_cvt_pk_bf16_f32 v41, v44, v45
	v_add_u32_e32 v42, 0xa0, v171
	v_cvt_pk_bf16_f32 v22, v22, v23
	v_cvt_pk_bf16_f32 v23, v24, v25
	v_cvt_pk_bf16_f32 v14, v14, v15
	v_cvt_pk_bf16_f32 v15, v16, v17
	v_add_u32_e32 v16, 0xd0, v171
	v_cvt_pk_bf16_f32 v58, v58, v59
	v_cvt_pk_bf16_f32 v59, v60, v61
	v_cvt_pk_bf16_f32 v54, v54, v55
	v_cvt_pk_bf16_f32 v55, v56, v57
	v_add_u32_e32 v56, 0x80, v171
	ds_write2st64_b64 v42, v[38:39], v[40:41] offset0:20 offset1:21
	v_cvt_pk_bf16_f32 v34, v34, v35
	v_cvt_pk_bf16_f32 v35, v36, v37
	v_cvt_pk_bf16_f32 v36, v46, v47
	v_cvt_pk_bf16_f32 v37, v48, v49
	v_add_u32_e32 v38, 0xb0, v171
	v_cvt_pk_bf16_f32 v30, v30, v31
	v_cvt_pk_bf16_f32 v31, v32, v33
	v_cvt_pk_bf16_f32 v26, v26, v27
	v_cvt_pk_bf16_f32 v27, v28, v29
	v_add_u32_e32 v28, 0xc0, v171
	ds_write2st64_b64 v16, v[22:23], v[14:15] offset0:26 offset1:27
	v_cvt_pk_bf16_f32 v14, v18, v19
	v_cvt_pk_bf16_f32 v15, v20, v21
	v_cvt_pk_bf16_f32 v10, v10, v11
	v_cvt_pk_bf16_f32 v11, v12, v13
	v_add_u32_e32 v12, 0xe0, v171
	v_cvt_pk_bf16_f32 v6, v6, v7
	v_cvt_pk_bf16_f32 v7, v8, v9
	v_cvt_pk_bf16_f32 v2, v2, v3
	v_cvt_pk_bf16_f32 v3, v4, v5
	v_add_u32_e32 v4, 0xf0, v171
	ds_write2st64_b64 v56, v[58:59], v[54:55] offset0:16 offset1:17
	ds_write2st64_b64 v38, v[34:35], v[36:37] offset0:22 offset1:23
	ds_write2st64_b64 v28, v[30:31], v[26:27] offset0:24 offset1:25
	ds_write2st64_b64 v12, v[14:15], v[10:11] offset0:28 offset1:29
	ds_write2st64_b64 v4, v[6:7], v[2:3] offset0:30 offset1:31
	v_add_u32_e32 v2, s31, v165
	v_min_i32_e32 v2, 0x18698, v2
	v_ashrrev_i32_e32 v3, 31, v2
	v_lshlrev_b64 v[2:3], 11, v[2:3]
	v_lshl_add_u64 v[2:3], v[162:163], 0, v[2:3]
	v_add_co_u32_e64 v4, s[22:23], s34, v2
	global_load_dwordx4 v[150:153], v[2:3], off nt
	global_load_dwordx4 v[142:145], v[2:3], off offset:1024 nt
	global_load_dwordx4 v[122:125], v[2:3], off offset:2048 nt
	global_load_dwordx4 v[110:113], v[2:3], off offset:3072 nt
	v_addc_co_u32_e64 v5, s[22:23], 0, v3, s[22:23]
	v_add_co_u32_e64 v6, s[22:23], s35, v2
	s_nop 1
	v_addc_co_u32_e64 v7, s[22:23], 0, v3, s[22:23]
	v_add_co_u32_e64 v2, s[22:23], s36, v2
	global_load_dwordx4 v[114:117], v[4:5], off offset:1024 nt
	global_load_dwordx4 v[98:101], v[4:5], off offset:2048 nt
	global_load_dwordx4 v[50:53], v[6:7], off nt
	global_load_dwordx4 v[38:41], v[6:7], off offset:1024 nt
	global_load_dwordx4 v[34:37], v[6:7], off offset:2048 nt
	global_load_dwordx4 v[26:29], v[6:7], off offset:3072 nt
	v_addc_co_u32_e64 v3, s[22:23], 0, v3, s[22:23]
	global_load_dwordx4 v[106:109], v[4:5], off offset:3072 nt
	global_load_dwordx4 v[30:33], v[2:3], off nt
	global_load_dwordx4 v[14:17], v[2:3], off offset:1024 nt
	global_load_dwordx4 v[10:13], v[2:3], off offset:2048 nt
	global_load_dwordx4 v[154:157], v[6:7], off offset:-4096 nt
	s_nop 0
	global_load_dwordx4 v[6:9], v[2:3], off offset:3072 nt
	v_mov_b32_e32 v2, 0x14500
	v_lshl_add_u32 v54, v183, 4, v2
	ds_read_b128 v[2:5], v54
	ds_read_b128 v[18:21], v54 offset:1024
	ds_read_b128 v[22:25], v168
	ds_read_b128 v[42:45], v168 offset:16
	s_waitcnt lgkmcnt(1)
	v_mfma_f32_16x16x32_bf16 v[2:5], v[2:5], v[22:25], 0
	ds_read_b128 v[22:25], v54 offset:2048
	ds_read_b128 v[46:49], v54 offset:3072
	s_waitcnt lgkmcnt(2)
	v_mfma_f32_16x16x32_bf16 v[2:5], v[18:21], v[42:45], v[2:5]
	ds_read_b128 v[18:21], v168 offset:32
	ds_read_b128 v[42:45], v168 offset:48
	s_waitcnt lgkmcnt(1)
	v_mfma_f32_16x16x32_bf16 v[2:5], v[22:25], v[18:21], v[2:5]
	s_waitcnt lgkmcnt(0)
	v_mfma_f32_16x16x32_bf16 v[2:5], v[46:49], v[42:45], v[2:5]
	ds_read_b128 v[18:21], v54 offset:4096
	ds_read_b128 v[22:25], v54 offset:5120
	ds_read_b128 v[42:45], v168 offset:64
	ds_read_b128 v[46:49], v168 offset:80
	s_waitcnt lgkmcnt(1)
	v_mfma_f32_16x16x32_bf16 v[2:5], v[18:21], v[42:45], v[2:5]
	ds_read_b128 v[18:21], v54 offset:6144
	ds_read_b128 v[42:45], v54 offset:7168
	s_waitcnt lgkmcnt(2)
	v_mfma_f32_16x16x32_bf16 v[2:5], v[22:25], v[46:49], v[2:5]
	ds_read_b128 v[22:25], v168 offset:96
	ds_read_b128 v[46:49], v168 offset:112
	s_waitcnt lgkmcnt(1)
	v_mfma_f32_16x16x32_bf16 v[2:5], v[18:21], v[22:25], v[2:5]
	s_waitcnt lgkmcnt(0)
	v_mfma_f32_16x16x32_bf16 v[2:5], v[42:45], v[46:49], v[2:5]
	ds_read_b128 v[18:21], v54 offset:8192
	ds_read_b128 v[22:25], v54 offset:9216
	ds_read_b128 v[42:45], v168 offset:128
	ds_read_b128 v[46:49], v168 offset:144
	s_waitcnt lgkmcnt(1)
	v_mfma_f32_16x16x32_bf16 v[2:5], v[18:21], v[42:45], v[2:5]
	ds_read_b128 v[18:21], v54 offset:10240
	ds_read_b128 v[42:45], v54 offset:11264
	s_waitcnt lgkmcnt(2)
	v_mfma_f32_16x16x32_bf16 v[2:5], v[22:25], v[46:49], v[2:5]
	ds_read_b128 v[22:25], v168 offset:160
	ds_read_b128 v[46:49], v168 offset:176
	s_waitcnt lgkmcnt(1)
	v_mfma_f32_16x16x32_bf16 v[2:5], v[18:21], v[22:25], v[2:5]
	s_waitcnt lgkmcnt(0)
	v_mfma_f32_16x16x32_bf16 v[2:5], v[42:45], v[46:49], v[2:5]
	ds_read_b128 v[18:21], v54 offset:12288
	ds_read_b128 v[22:25], v54 offset:13312
	ds_read_b128 v[42:45], v168 offset:192
	ds_read_b128 v[46:49], v168 offset:208
	s_waitcnt lgkmcnt(1)
	v_mfma_f32_16x16x32_bf16 v[2:5], v[18:21], v[42:45], v[2:5]
	ds_read_b128 v[18:21], v54 offset:14336
	ds_read_b128 v[42:45], v54 offset:15360
	s_waitcnt lgkmcnt(2)
	v_mfma_f32_16x16x32_bf16 v[2:5], v[22:25], v[46:49], v[2:5]
	ds_read_b128 v[22:25], v168 offset:224
	ds_read_b128 v[46:49], v168 offset:240
	s_waitcnt lgkmcnt(1)
	v_mfma_f32_16x16x32_bf16 v[2:5], v[18:21], v[22:25], v[2:5]
	s_waitcnt lgkmcnt(0)
	v_mfma_f32_16x16x32_bf16 v[2:5], v[42:45], v[46:49], v[2:5]
	s_waitcnt vmcnt(42)
	v_cmp_ne_u16_e64 s[22:23], -1, v181
	s_and_b64 s[22:23], s[18:19], s[22:23]
	s_and_saveexec_b64 s[18:19], s[22:23]
	v_and_b32_e32 v18, 0xffff, v181
	v_mov_b32_e32 v19, 0x18500
	v_lshl_add_u32 v18, v18, 2, v19
	v_mov_b32_e32 v19, 1
	ds_add_u32 v18, v19
	s_or_b64 exec, exec, s[18:19]
	v_mov_b32_e32 v18, 0xffff
	s_mov_b32 s22, 0xffff
	s_waitcnt vmcnt(41)
	v_cndmask_b32_sdwa v19, v18, v178, vcc dst_sel:DWORD dst_unused:UNUSED_PAD src0_sel:DWORD src1_sel:WORD_0
	v_cmp_ne_u32_e32 vcc, s22, v19
	s_and_saveexec_b64 s[18:19], vcc
	v_mov_b32_e32 v20, 0x18500
	v_lshl_add_u32 v19, v19, 2, v20
	v_mov_b32_e32 v20, 1
	ds_add_u32 v19, v20
	s_or_b64 exec, exec, s[18:19]
	s_mov_b64 vcc, s[8:9]
	s_waitcnt vmcnt(40)
	v_cndmask_b32_sdwa v18, v18, v176, vcc dst_sel:DWORD dst_unused:UNUSED_PAD src0_sel:DWORD src1_sel:WORD_0
	v_cmp_ne_u32_e32 vcc, s22, v18
	s_and_saveexec_b64 s[8:9], vcc
	v_mov_b32_e32 v19, 0x18500
	v_lshl_add_u32 v18, v18, 2, v19
	v_mov_b32_e32 v19, 1
	ds_add_u32 v18, v19
	s_or_b64 exec, exec, s[8:9]
	s_mov_b64 vcc, s[4:5]
	v_mov_b32_e32 v18, 0xffff
	s_mov_b32 s8, 0xffff
	s_waitcnt vmcnt(39)
	v_cndmask_b32_sdwa v19, v18, v172, vcc dst_sel:DWORD dst_unused:UNUSED_PAD src0_sel:DWORD src1_sel:WORD_0
	v_cmp_ne_u32_e32 vcc, s8, v19
	s_and_saveexec_b64 s[4:5], vcc
	v_mov_b32_e32 v20, 0x18500
	v_lshl_add_u32 v19, v19, 2, v20
	v_mov_b32_e32 v20, 1
	ds_add_u32 v19, v20
	s_or_b64 exec, exec, s[4:5]
	s_mov_b64 vcc, s[20:21]
	s_waitcnt vmcnt(38)
	v_cndmask_b32_sdwa v18, v18, v182, vcc dst_sel:DWORD dst_unused:UNUSED_PAD src0_sel:DWORD src1_sel:WORD_0
	v_cmp_ne_u32_e32 vcc, s8, v18
	s_and_saveexec_b64 s[4:5], vcc
	v_mov_b32_e32 v19, 0x18500
	v_lshl_add_u32 v18, v18, 2, v19
	v_mov_b32_e32 v19, 1
	ds_add_u32 v18, v19
	s_or_b64 exec, exec, s[4:5]
	s_mov_b64 vcc, s[16:17]
	v_mov_b32_e32 v18, 0xffff
	s_waitcnt vmcnt(37)
	v_cndmask_b32_sdwa v19, v18, v179, vcc dst_sel:DWORD dst_unused:UNUSED_PAD src0_sel:DWORD src1_sel:WORD_0
	v_cmp_ne_u32_e32 vcc, s8, v19
	s_and_saveexec_b64 s[4:5], vcc
	v_mov_b32_e32 v20, 0x18500
	v_lshl_add_u32 v19, v19, 2, v20
	v_mov_b32_e32 v20, 1
	ds_add_u32 v19, v20
	s_or_b64 exec, exec, s[4:5]
	s_mov_b64 vcc, s[10:11]
	s_waitcnt vmcnt(36)
	v_cndmask_b32_sdwa v18, v18, v177, vcc dst_sel:DWORD dst_unused:UNUSED_PAD src0_sel:DWORD src1_sel:WORD_0
	v_cmp_ne_u32_e32 vcc, s8, v18
	s_and_saveexec_b64 s[4:5], vcc
	v_mov_b32_e32 v19, 0x18500
	v_lshl_add_u32 v18, v18, 2, v19
	v_mov_b32_e32 v19, 1
	ds_add_u32 v18, v19
	s_or_b64 exec, exec, s[4:5]
	s_mov_b64 vcc, s[6:7]
	v_mov_b32_e32 v18, 0xffff
	s_mov_b32 s6, 0xffff
	s_waitcnt vmcnt(35)
	v_cndmask_b32_sdwa v19, v18, v173, vcc dst_sel:DWORD dst_unused:UNUSED_PAD src0_sel:DWORD src1_sel:WORD_0
	v_cmp_ne_u32_e32 vcc, s6, v19
	s_and_saveexec_b64 s[4:5], vcc
	v_mov_b32_e32 v20, 0x18500
	v_lshl_add_u32 v19, v19, 2, v20
	v_mov_b32_e32 v20, 1
	ds_add_u32 v19, v20
	s_or_b64 exec, exec, s[4:5]
	s_mov_b64 vcc, s[14:15]
	s_waitcnt vmcnt(34)
	v_cndmask_b32_sdwa v18, v18, v180, vcc dst_sel:DWORD dst_unused:UNUSED_PAD src0_sel:DWORD src1_sel:WORD_0
	v_cmp_ne_u32_e32 vcc, s6, v18
	s_and_saveexec_b64 s[4:5], vcc
	v_mov_b32_e32 v19, 0x18500
	v_lshl_add_u32 v18, v18, 2, v19
	v_mov_b32_e32 v19, 1
	ds_add_u32 v18, v19
	s_or_b64 exec, exec, s[4:5]
	s_mov_b64 vcc, s[12:13]
	v_mov_b32_e32 v18, 0xffff
	s_waitcnt vmcnt(33)
	v_cndmask_b32_sdwa v19, v18, v175, vcc dst_sel:DWORD dst_unused:UNUSED_PAD src0_sel:DWORD src1_sel:WORD_0
	v_cmp_ne_u32_e32 vcc, s6, v19
	s_and_saveexec_b64 s[4:5], vcc
	v_mov_b32_e32 v20, 0x18500
	v_lshl_add_u32 v19, v19, 2, v20
	v_mov_b32_e32 v20, 1
	ds_add_u32 v19, v20
	s_or_b64 exec, exec, s[4:5]
	s_mov_b64 vcc, s[0:1]
	s_waitcnt vmcnt(32)
	v_cndmask_b32_sdwa v18, v18, v174, vcc dst_sel:DWORD dst_unused:UNUSED_PAD src0_sel:DWORD src1_sel:WORD_0
	v_cmp_ne_u32_e32 vcc, s6, v18
	s_and_saveexec_b64 s[0:1], vcc
	v_mov_b32_e32 v19, 0x18500
	v_lshl_add_u32 v18, v18, 2, v19
	v_mov_b32_e32 v19, 1
	ds_add_u32 v18, v19
	s_or_b64 exec, exec, s[0:1]
	v_mov_b32_e32 v183, v1
	ds_read2_b32 v[18:19], v169 offset0:55 offset1:60
	ds_read2_b32 v[20:21], v170 offset0:55 offset1:60
	ds_read2_b32 v[22:23], v170 offset0:65 offset1:70
	ds_read2_b32 v[24:25], v169 offset0:65 offset1:70
	v_mov_b32_e32 v43, 0
	s_waitcnt lgkmcnt(3)
	v_add_u32_e32 v18, v18, v1
	s_waitcnt lgkmcnt(2)
	v_cmp_lt_u32_e64 s[20:21], v1, v20
	s_waitcnt lgkmcnt(1)
	v_cmp_lt_u32_e64 s[16:17], v1, v22
	s_waitcnt lgkmcnt(0)
	v_add_u32_e32 v20, v24, v1
	v_add_u32_e32 v22, v25, v1
	ds_read2_b32 v[24:25], v169 offset0:75 offset1:80
	ds_read2_b32 v[46:47], v170 offset0:75 offset1:80
	v_cndmask_b32_e64 v42, 0, v18, s[20:21]
	v_add_u32_e32 v18, v19, v1
	v_cmp_lt_u32_e32 vcc, v1, v21
	v_lshl_add_u64 v[44:45], v[42:43], 1, s[26:27]
	v_cmp_lt_u32_e64 s[18:19], v1, v23
	v_cndmask_b32_e32 v42, 0, v18, vcc
	v_lshl_add_u64 v[18:19], v[42:43], 1, s[26:27]
	v_cndmask_b32_e64 v42, 0, v20, s[16:17]
	v_lshl_add_u64 v[20:21], v[42:43], 1, s[26:27]
	v_cndmask_b32_e64 v42, 0, v22, s[18:19]
	s_waitcnt lgkmcnt(1)
	v_add_u32_e32 v24, v24, v1
	s_waitcnt lgkmcnt(0)
	v_cmp_lt_u32_e64 s[12:13], v1, v46
	v_lshl_add_u64 v[22:23], v[42:43], 1, s[26:27]
	v_cmp_lt_u32_e64 s[14:15], v1, v47
	v_cndmask_b32_e64 v42, 0, v24, s[12:13]
	v_lshl_add_u64 v[48:49], v[42:43], 1, s[26:27]
	v_add_u32_e32 v42, v25, v1
	ds_read2_b32 v[24:25], v169 offset0:85 offset1:90
	ds_read2_b32 v[54:55], v170 offset0:85 offset1:90
	v_cndmask_b32_e64 v42, 0, v42, s[14:15]
	v_lshl_add_u64 v[46:47], v[42:43], 1, s[26:27]
	s_waitcnt lgkmcnt(1)
	v_add_u32_e32 v24, v24, v1
	s_waitcnt lgkmcnt(0)
	v_cmp_lt_u32_e64 s[10:11], v1, v54
	v_cmp_lt_u32_e64 s[4:5], v1, v55
	ds_read2_b32 v[54:55], v169 offset0:95 offset1:100
	ds_read2_b32 v[58:59], v170 offset0:95 offset1:100
	v_cndmask_b32_e64 v42, 0, v24, s[10:11]
	v_add_u32_e32 v24, v25, v1
	v_lshl_add_u64 v[56:57], v[42:43], 1, s[26:27]
	v_cndmask_b32_e64 v42, 0, v24, s[4:5]
	v_lshl_add_u64 v[24:25], v[42:43], 1, s[26:27]
	global_load_ushort v182, v[44:45], off
	global_load_ushort v181, v[18:19], off
	global_load_ushort v180, v[20:21], off
	global_load_ushort v179, v[22:23], off
	global_load_ushort v178, v[48:49], off
	global_load_ushort v177, v[46:47], off
	global_load_ushort v176, v[56:57], off
	global_load_ushort v174, v[24:25], off
	ds_read_b32 v22, v169 offset:420
	ds_read_b32 v23, v170 offset:420
	s_waitcnt lgkmcnt(3)
	v_add_u32_e32 v18, v54, v1
	s_waitcnt lgkmcnt(2)
	v_cmp_lt_u32_e64 s[6:7], v1, v58
	v_add_u32_e32 v20, v55, v1
	v_cmp_lt_u32_e64 s[8:9], v1, v59
	v_cndmask_b32_e64 v42, 0, v18, s[6:7]
	v_lshl_add_u64 v[18:19], v[42:43], 1, s[26:27]
	v_cndmask_b32_e64 v42, 0, v20, s[8:9]
	s_waitcnt lgkmcnt(1)
	v_add_u32_e32 v22, v22, v1
	s_waitcnt lgkmcnt(0)
	v_cmp_lt_u32_e64 s[0:1], v1, v23
	v_lshl_add_u64 v[20:21], v[42:43], 1, s[26:27]
	s_nop 0
	v_cndmask_b32_e64 v42, 0, v22, s[0:1]
	v_lshl_add_u64 v[22:23], v[42:43], 1, s[26:27]
	global_load_ushort v175, v[18:19], off
	global_load_ushort v173, v[20:21], off
	global_load_ushort v172, v[22:23], off
	s_waitcnt vmcnt(42)
	v_cvt_pk_bf16_f32 v18, v146, v147
	v_cvt_pk_bf16_f32 v19, v148, v149
	s_waitcnt vmcnt(41)
	v_cvt_pk_bf16_f32 v20, v138, v139
	v_cvt_pk_bf16_f32 v21, v140, v141
	ds_write2st64_b64 v171, v[18:19], v[20:21] offset1:1
	s_waitcnt vmcnt(40)
	v_cvt_pk_bf16_f32 v18, v126, v127
	v_cvt_pk_bf16_f32 v19, v128, v129
	s_waitcnt vmcnt(39)
	v_cvt_pk_bf16_f32 v20, v118, v119
	v_cvt_pk_bf16_f32 v21, v120, v121
	ds_write2_b64 v171, v[18:19], v[20:21] offset0:130 offset1:194
	s_waitcnt vmcnt(28)
	v_cvt_pk_bf16_f32 v18, v158, v159
	v_cvt_pk_bf16_f32 v19, v160, v161
	v_cvt_pk_bf16_f32 v20, v130, v131
	v_cvt_pk_bf16_f32 v21, v132, v133
	v_add_u32_e32 v22, 32, v171
	ds_write2st64_b64 v22, v[18:19], v[20:21] offset0:4 offset1:5
	v_cvt_pk_bf16_f32 v18, v102, v103
	v_cvt_pk_bf16_f32 v19, v104, v105
	v_cvt_pk_bf16_f32 v20, v134, v135
	v_cvt_pk_bf16_f32 v21, v136, v137
	v_add_u32_e32 v22, 48, v171
	ds_write2st64_b64 v22, v[18:19], v[20:21] offset0:6 offset1:7
	v_cvt_pk_bf16_f32 v18, v94, v95
	v_cvt_pk_bf16_f32 v19, v96, v97
	v_cvt_pk_bf16_f32 v20, v90, v91
	v_cvt_pk_bf16_f32 v21, v92, v93
	v_add_u32_e32 v22, 64, v171
	ds_write2st64_b64 v22, v[18:19], v[20:21] offset0:8 offset1:9
	v_cvt_pk_bf16_f32 v18, v86, v87
	v_cvt_pk_bf16_f32 v19, v88, v89
	v_cvt_pk_bf16_f32 v20, v78, v79
	v_cvt_pk_bf16_f32 v21, v80, v81
	v_add_u32_e32 v22, 0x50, v171
	ds_write2st64_b64 v22, v[18:19], v[20:21] offset0:10 offset1:11
	v_cvt_pk_bf16_f32 v18, v82, v83
	v_cvt_pk_bf16_f32 v19, v84, v85
	v_cvt_pk_bf16_f32 v20, v74, v75
	v_cvt_pk_bf16_f32 v21, v76, v77
	v_add_u32_e32 v22, 0x60, v171
	ds_write2st64_b64 v22, v[18:19], v[20:21] offset0:12 offset1:13
	v_cvt_pk_bf16_f32 v18, v70, v71
	v_cvt_pk_bf16_f32 v19, v72, v73
	s_waitcnt vmcnt(27)
	v_cvt_pk_bf16_f32 v20, v66, v67
	v_cvt_pk_bf16_f32 v21, v68, v69
	v_add_u32_e32 v22, 0x70, v171
	ds_write2st64_b64 v22, v[18:19], v[20:21] offset0:14 offset1:15
	v_mov_b32_e32 v18, 0x50
	v_lshl_add_u32 v158, v164, 4, v18
	v_add_u32_e32 v18, s33, v158
	v_min_i32_e32 v18, 0x18698, v18
	v_ashrrev_i32_e32 v19, 31, v18
	v_lshlrev_b64 v[18:19], 11, v[18:19]
	v_lshl_add_u64 v[18:19], v[162:163], 0, v[18:19]
	v_add_co_u32_e64 v20, s[22:23], s34, v18
	global_load_dwordx4 v[134:137], v[18:19], off nt
	global_load_dwordx4 v[130:133], v[18:19], off offset:1024 nt
	global_load_dwordx4 v[102:105], v[18:19], off offset:2048 nt
	global_load_dwordx4 v[90:93], v[18:19], off offset:3072 nt
	v_addc_co_u32_e64 v21, s[22:23], 0, v19, s[22:23]
	v_add_co_u32_e64 v66, s[22:23], s35, v18
	s_nop 1
	v_addc_co_u32_e64 v67, s[22:23], 0, v19, s[22:23]
	v_add_co_u32_e64 v18, s[22:23], s36, v18
	global_load_dwordx4 v[118:121], v[20:21], off offset:1024 nt
	global_load_dwordx4 v[78:81], v[20:21], off offset:2048 nt
	global_load_dwordx4 v[74:77], v[66:67], off nt
	global_load_dwordx4 v[62:65], v[66:67], off offset:1024 nt
	global_load_dwordx4 v[58:61], v[66:67], off offset:2048 nt
	global_load_dwordx4 v[46:49], v[66:67], off offset:3072 nt
	v_addc_co_u32_e64 v19, s[22:23], 0, v19, s[22:23]
	global_load_dwordx4 v[126:129], v[20:21], off offset:3072 nt
	global_load_dwordx4 v[54:57], v[18:19], off nt
	global_load_dwordx4 v[42:45], v[18:19], off offset:1024 nt
	global_load_dwordx4 v[22:25], v[18:19], off offset:2048 nt
	global_load_dwordx4 v[146:149], v[66:67], off offset:-4096 nt
	s_nop 0
	global_load_dwordx4 v[18:21], v[18:19], off offset:3072 nt
	s_waitcnt vmcnt(42)
	v_cvt_pk_bf16_f32 v66, v150, v151
	v_cvt_pk_bf16_f32 v67, v152, v153
	s_waitcnt vmcnt(41)
	v_cvt_pk_bf16_f32 v68, v142, v143
	v_cvt_pk_bf16_f32 v69, v144, v145
	v_add_u32_e32 v70, 0x80, v171
	ds_write2st64_b64 v70, v[66:67], v[68:69] offset0:16 offset1:17
	s_waitcnt vmcnt(40)
	v_cvt_pk_bf16_f32 v66, v122, v123
	v_cvt_pk_bf16_f32 v67, v124, v125
	s_waitcnt vmcnt(39)
	v_cvt_pk_bf16_f32 v68, v110, v111
	v_cvt_pk_bf16_f32 v69, v112, v113
	v_add_u32_e32 v70, 0x90, v171
	ds_write2st64_b64 v70, v[66:67], v[68:69] offset0:18 offset1:19
	s_waitcnt vmcnt(28)
	v_cvt_pk_bf16_f32 v66, v154, v155
	v_cvt_pk_bf16_f32 v67, v156, v157
	v_cvt_pk_bf16_f32 v68, v114, v115
	v_cvt_pk_bf16_f32 v69, v116, v117
	v_add_u32_e32 v70, 0xa0, v171
	v_cvt_pk_bf16_f32 v34, v34, v35
	v_cvt_pk_bf16_f32 v35, v36, v37
	v_cvt_pk_bf16_f32 v26, v26, v27
	v_cvt_pk_bf16_f32 v27, v28, v29
	v_add_u32_e32 v28, 0xd0, v171
	ds_write2st64_b64 v70, v[66:67], v[68:69] offset0:20 offset1:21
	v_cvt_pk_bf16_f32 v66, v98, v99
	v_cvt_pk_bf16_f32 v67, v100, v101
	v_cvt_pk_bf16_f32 v68, v106, v107
	v_cvt_pk_bf16_f32 v69, v108, v109
	v_add_u32_e32 v70, 0xb0, v171
	v_cvt_pk_bf16_f32 v50, v50, v51
	v_cvt_pk_bf16_f32 v51, v52, v53
	v_cvt_pk_bf16_f32 v38, v38, v39
	v_cvt_pk_bf16_f32 v39, v40, v41
	v_add_u32_e32 v40, 0xc0, v171
	ds_write2st64_b64 v28, v[34:35], v[26:27] offset0:26 offset1:27
	v_cvt_pk_bf16_f32 v26, v30, v31
	v_cvt_pk_bf16_f32 v27, v32, v33
	v_cvt_pk_bf16_f32 v14, v14, v15
	v_cvt_pk_bf16_f32 v15, v16, v17
	v_add_u32_e32 v16, 0xe0, v171
	v_cvt_pk_bf16_f32 v10, v10, v11
	v_cvt_pk_bf16_f32 v11, v12, v13
	s_waitcnt vmcnt(27)
	v_cvt_pk_bf16_f32 v6, v6, v7
	v_cvt_pk_bf16_f32 v7, v8, v9
	v_add_u32_e32 v8, 0xf0, v171
	ds_write2st64_b64 v70, v[66:67], v[68:69] offset0:22 offset1:23
	ds_write2st64_b64 v40, v[50:51], v[38:39] offset0:24 offset1:25
	ds_write2st64_b64 v16, v[26:27], v[14:15] offset0:28 offset1:29
	ds_write2st64_b64 v8, v[10:11], v[6:7] offset0:30 offset1:31
	v_add_u32_e32 v6, s31, v158
	v_min_i32_e32 v6, 0x18698, v6
	v_ashrrev_i32_e32 v7, 31, v6
	v_lshlrev_b64 v[6:7], 11, v[6:7]
	v_lshl_add_u64 v[6:7], v[162:163], 0, v[6:7]
	v_add_co_u32_e64 v8, s[22:23], s34, v6
	global_load_dwordx4 v[138:141], v[6:7], off nt
	global_load_dwordx4 v[114:117], v[6:7], off offset:1024 nt
	global_load_dwordx4 v[106:109], v[6:7], off offset:2048 nt
	global_load_dwordx4 v[94:97], v[6:7], off offset:3072 nt
	v_addc_co_u32_e64 v9, s[22:23], 0, v7, s[22:23]
	v_add_co_u32_e64 v10, s[22:23], s35, v6
	s_nop 1
	v_addc_co_u32_e64 v11, s[22:23], 0, v7, s[22:23]
	v_add_co_u32_e64 v6, s[22:23], s36, v6
	global_load_dwordx4 v[98:101], v[8:9], off offset:1024 nt
	global_load_dwordx4 v[82:85], v[8:9], off offset:2048 nt
	global_load_dwordx4 v[70:73], v[10:11], off nt
	global_load_dwordx4 v[66:69], v[10:11], off offset:1024 nt
	global_load_dwordx4 v[50:53], v[10:11], off offset:2048 nt
	global_load_dwordx4 v[34:37], v[10:11], off offset:3072 nt
	v_addc_co_u32_e64 v7, s[22:23], 0, v7, s[22:23]
	global_load_dwordx4 v[86:89], v[8:9], off offset:3072 nt
	global_load_dwordx4 v[38:41], v[6:7], off nt
	global_load_dwordx4 v[26:29], v[6:7], off offset:1024 nt
	global_load_dwordx4 v[14:17], v[6:7], off offset:2048 nt
	global_load_dwordx4 v[142:145], v[10:11], off offset:-4096 nt
	s_nop 0
	global_load_dwordx4 v[10:13], v[6:7], off offset:3072 nt
	v_mov_b32_e32 v6, 0x14500
	v_lshl_add_u32 v154, v183, 4, v6
	ds_read_b128 v[6:9], v154
	ds_read_b128 v[30:33], v154 offset:1024
	ds_read_b128 v[110:113], v168
	ds_read_b128 v[122:125], v168 offset:16
	s_waitcnt lgkmcnt(1)
	v_mfma_f32_16x16x32_bf16 v[6:9], v[6:9], v[110:113], 0
	ds_read_b128 v[110:113], v154 offset:2048
	ds_read_b128 v[150:153], v154 offset:3072
	s_waitcnt lgkmcnt(2)
	v_mfma_f32_16x16x32_bf16 v[6:9], v[30:33], v[122:125], v[6:9]
	ds_read_b128 v[30:33], v168 offset:32
	ds_read_b128 v[122:125], v168 offset:48
	s_waitcnt lgkmcnt(1)
	v_mfma_f32_16x16x32_bf16 v[6:9], v[110:113], v[30:33], v[6:9]
	s_waitcnt lgkmcnt(0)
	v_mfma_f32_16x16x32_bf16 v[6:9], v[150:153], v[122:125], v[6:9]
	ds_read_b128 v[30:33], v154 offset:4096
	ds_read_b128 v[110:113], v154 offset:5120
	ds_read_b128 v[122:125], v168 offset:64
	ds_read_b128 v[150:153], v168 offset:80
	s_waitcnt lgkmcnt(1)
	v_mfma_f32_16x16x32_bf16 v[6:9], v[30:33], v[122:125], v[6:9]
	ds_read_b128 v[30:33], v154 offset:6144
	ds_read_b128 v[122:125], v154 offset:7168
	s_waitcnt lgkmcnt(2)
	v_mfma_f32_16x16x32_bf16 v[6:9], v[110:113], v[150:153], v[6:9]
	ds_read_b128 v[110:113], v168 offset:96
	ds_read_b128 v[150:153], v168 offset:112
	s_waitcnt lgkmcnt(1)
	v_mfma_f32_16x16x32_bf16 v[6:9], v[30:33], v[110:113], v[6:9]
	s_waitcnt lgkmcnt(0)
	v_mfma_f32_16x16x32_bf16 v[6:9], v[122:125], v[150:153], v[6:9]
	ds_read_b128 v[30:33], v154 offset:8192
	ds_read_b128 v[110:113], v154 offset:9216
	ds_read_b128 v[122:125], v168 offset:128
	ds_read_b128 v[150:153], v168 offset:144
	s_waitcnt lgkmcnt(1)
	v_mfma_f32_16x16x32_bf16 v[6:9], v[30:33], v[122:125], v[6:9]
	ds_read_b128 v[30:33], v154 offset:10240
	ds_read_b128 v[122:125], v154 offset:11264
	s_waitcnt lgkmcnt(2)
	v_mfma_f32_16x16x32_bf16 v[6:9], v[110:113], v[150:153], v[6:9]
	ds_read_b128 v[110:113], v168 offset:160
	ds_read_b128 v[150:153], v168 offset:176
	s_waitcnt lgkmcnt(1)
	v_mfma_f32_16x16x32_bf16 v[6:9], v[30:33], v[110:113], v[6:9]
	s_waitcnt lgkmcnt(0)
	v_mfma_f32_16x16x32_bf16 v[6:9], v[122:125], v[150:153], v[6:9]
	ds_read_b128 v[30:33], v154 offset:12288
	ds_read_b128 v[110:113], v154 offset:13312
	ds_read_b128 v[122:125], v168 offset:192
	ds_read_b128 v[150:153], v168 offset:208
	s_waitcnt lgkmcnt(1)
	v_mfma_f32_16x16x32_bf16 v[6:9], v[30:33], v[122:125], v[6:9]
	ds_read_b128 v[30:33], v154 offset:14336
	ds_read_b128 v[122:125], v154 offset:15360
	s_waitcnt lgkmcnt(2)
	v_mfma_f32_16x16x32_bf16 v[6:9], v[110:113], v[150:153], v[6:9]
	ds_read_b128 v[110:113], v168 offset:224
	ds_read_b128 v[150:153], v168 offset:240
	s_waitcnt lgkmcnt(1)
	v_mfma_f32_16x16x32_bf16 v[6:9], v[30:33], v[110:113], v[6:9]
	s_waitcnt lgkmcnt(0)
	v_mfma_f32_16x16x32_bf16 v[6:9], v[122:125], v[150:153], v[6:9]
	s_waitcnt vmcnt(42)
	v_cmp_ne_u16_e64 s[22:23], -1, v182
	s_and_b64 s[22:23], s[20:21], s[22:23]
	s_and_saveexec_b64 s[20:21], s[22:23]
	v_and_b32_e32 v30, 0xffff, v182
	v_mov_b32_e32 v31, 0x18500
	v_lshl_add_u32 v30, v30, 2, v31
	v_mov_b32_e32 v31, 1
	ds_add_u32 v30, v31
	s_or_b64 exec, exec, s[20:21]
	v_mov_b32_e32 v30, 0xffff
	s_mov_b32 s22, 0xffff
	s_waitcnt vmcnt(41)
	v_cndmask_b32_sdwa v31, v30, v181, vcc dst_sel:DWORD dst_unused:UNUSED_PAD src0_sel:DWORD src1_sel:WORD_0
	v_cmp_ne_u32_e32 vcc, s22, v31
	s_and_saveexec_b64 s[20:21], vcc
	v_mov_b32_e32 v32, 0x18500
	v_lshl_add_u32 v31, v31, 2, v32
	v_mov_b32_e32 v32, 1
	ds_add_u32 v31, v32
	s_or_b64 exec, exec, s[20:21]
	s_mov_b64 vcc, s[16:17]
	s_waitcnt vmcnt(40)
	v_cndmask_b32_sdwa v30, v30, v180, vcc dst_sel:DWORD dst_unused:UNUSED_PAD src0_sel:DWORD src1_sel:WORD_0
	v_cmp_ne_u32_e32 vcc, s22, v30
	s_and_saveexec_b64 s[16:17], vcc
	v_mov_b32_e32 v31, 0x18500
	v_lshl_add_u32 v30, v30, 2, v31
	v_mov_b32_e32 v31, 1
	ds_add_u32 v30, v31
	s_or_b64 exec, exec, s[16:17]
	s_mov_b64 vcc, s[18:19]
	v_mov_b32_e32 v30, 0xffff
	s_mov_b32 s18, 0xffff
	s_waitcnt vmcnt(39)
	v_cndmask_b32_sdwa v31, v30, v179, vcc dst_sel:DWORD dst_unused:UNUSED_PAD src0_sel:DWORD src1_sel:WORD_0
	v_cmp_ne_u32_e32 vcc, s18, v31
	s_and_saveexec_b64 s[16:17], vcc
	v_mov_b32_e32 v32, 0x18500
	v_lshl_add_u32 v31, v31, 2, v32
	v_mov_b32_e32 v32, 1
	ds_add_u32 v31, v32
	s_or_b64 exec, exec, s[16:17]
	s_mov_b64 vcc, s[12:13]
	s_waitcnt vmcnt(38)
	v_cndmask_b32_sdwa v30, v30, v178, vcc dst_sel:DWORD dst_unused:UNUSED_PAD src0_sel:DWORD src1_sel:WORD_0
	v_cmp_ne_u32_e32 vcc, s18, v30
	s_and_saveexec_b64 s[12:13], vcc
	v_mov_b32_e32 v31, 0x18500
	v_lshl_add_u32 v30, v30, 2, v31
	v_mov_b32_e32 v31, 1
	ds_add_u32 v30, v31
	s_or_b64 exec, exec, s[12:13]
	s_mov_b64 vcc, s[14:15]
	v_mov_b32_e32 v30, 0xffff
	s_mov_b32 s14, 0xffff
	s_waitcnt vmcnt(37)
	v_cndmask_b32_sdwa v31, v30, v177, vcc dst_sel:DWORD dst_unused:UNUSED_PAD src0_sel:DWORD src1_sel:WORD_0
	v_cmp_ne_u32_e32 vcc, s14, v31
	s_and_saveexec_b64 s[12:13], vcc
	v_mov_b32_e32 v32, 0x18500
	v_lshl_add_u32 v31, v31, 2, v32
	v_mov_b32_e32 v32, 1
	ds_add_u32 v31, v32
	s_or_b64 exec, exec, s[12:13]
	s_mov_b64 vcc, s[10:11]
	s_waitcnt vmcnt(36)
	v_cndmask_b32_sdwa v30, v30, v176, vcc dst_sel:DWORD dst_unused:UNUSED_PAD src0_sel:DWORD src1_sel:WORD_0
	v_cmp_ne_u32_e32 vcc, s14, v30
	s_and_saveexec_b64 s[10:11], vcc
	v_mov_b32_e32 v31, 0x18500
	v_lshl_add_u32 v30, v30, 2, v31
	v_mov_b32_e32 v31, 1
	ds_add_u32 v30, v31
	s_or_b64 exec, exec, s[10:11]
	s_mov_b64 vcc, s[4:5]
	v_mov_b32_e32 v30, 0xffff
	s_mov_b32 s10, 0xffff
	s_waitcnt vmcnt(35)
	v_cndmask_b32_sdwa v31, v30, v174, vcc dst_sel:DWORD dst_unused:UNUSED_PAD src0_sel:DWORD src1_sel:WORD_0
	v_cmp_ne_u32_e32 vcc, s10, v31
	s_and_saveexec_b64 s[4:5], vcc
	v_mov_b32_e32 v32, 0x18500
	v_lshl_add_u32 v31, v31, 2, v32
	v_mov_b32_e32 v32, 1
	ds_add_u32 v31, v32
	s_or_b64 exec, exec, s[4:5]
	s_mov_b64 vcc, s[6:7]
	s_waitcnt vmcnt(34)
	v_cndmask_b32_sdwa v30, v30, v175, vcc dst_sel:DWORD dst_unused:UNUSED_PAD src0_sel:DWORD src1_sel:WORD_0
	v_cmp_ne_u32_e32 vcc, s10, v30
	s_and_saveexec_b64 s[4:5], vcc
	v_mov_b32_e32 v31, 0x18500
	v_lshl_add_u32 v30, v30, 2, v31
	v_mov_b32_e32 v31, 1
	ds_add_u32 v30, v31
	s_or_b64 exec, exec, s[4:5]
	s_mov_b64 vcc, s[8:9]
	v_mov_b32_e32 v30, 0xffff
	s_mov_b32 s6, 0xffff
	s_waitcnt vmcnt(33)
	v_cndmask_b32_sdwa v31, v30, v173, vcc dst_sel:DWORD dst_unused:UNUSED_PAD src0_sel:DWORD src1_sel:WORD_0
	v_cmp_ne_u32_e32 vcc, s6, v31
	s_and_saveexec_b64 s[4:5], vcc
	v_mov_b32_e32 v32, 0x18500
	v_lshl_add_u32 v31, v31, 2, v32
	v_mov_b32_e32 v32, 1
	ds_add_u32 v31, v32
	s_or_b64 exec, exec, s[4:5]
	s_mov_b64 vcc, s[0:1]
	s_waitcnt vmcnt(32)
	v_cndmask_b32_sdwa v30, v30, v172, vcc dst_sel:DWORD dst_unused:UNUSED_PAD src0_sel:DWORD src1_sel:WORD_0
	v_cmp_ne_u32_e32 vcc, s6, v30
	s_and_saveexec_b64 s[0:1], vcc
	v_mov_b32_e32 v31, 0x18500
	v_lshl_add_u32 v30, v30, 2, v31
	v_mov_b32_e32 v31, 1
	ds_add_u32 v30, v31
	s_or_b64 exec, exec, s[0:1]
	v_mov_b32_e32 v173, v1
	ds_read2_b32 v[30:31], v169 offset0:110 offset1:115
	ds_read2_b32 v[32:33], v170 offset0:110 offset1:115
	ds_read2_b32 v[110:111], v170 offset0:120 offset1:125
	ds_read2_b32 v[112:113], v169 offset0:120 offset1:125
	v_mov_b32_e32 v123, 0
	s_waitcnt lgkmcnt(3)
	v_add_u32_e32 v30, v30, v1
	s_waitcnt lgkmcnt(2)
	v_cmp_lt_u32_e64 s[20:21], v1, v32
	s_waitcnt lgkmcnt(1)
	v_cmp_lt_u32_e64 s[16:17], v1, v110
	s_waitcnt lgkmcnt(0)
	v_add_u32_e32 v32, v112, v1
	v_add_u32_e32 v110, v113, v1
	ds_read2_b32 v[112:113], v169 offset0:130 offset1:135
	ds_read2_b32 v[150:151], v170 offset0:130 offset1:135
	v_cndmask_b32_e64 v122, 0, v30, s[20:21]
	v_add_u32_e32 v30, v31, v1
	v_cmp_lt_u32_e32 vcc, v1, v33
	v_lshl_add_u64 v[124:125], v[122:123], 1, s[26:27]
	v_cmp_lt_u32_e64 s[18:19], v1, v111
	v_cndmask_b32_e32 v122, 0, v30, vcc
	v_lshl_add_u64 v[30:31], v[122:123], 1, s[26:27]
	v_cndmask_b32_e64 v122, 0, v32, s[16:17]
	v_lshl_add_u64 v[32:33], v[122:123], 1, s[26:27]
	v_cndmask_b32_e64 v122, 0, v110, s[18:19]
	s_waitcnt lgkmcnt(1)
	v_add_u32_e32 v112, v112, v1
	s_waitcnt lgkmcnt(0)
	v_cmp_lt_u32_e64 s[12:13], v1, v150
	v_lshl_add_u64 v[110:111], v[122:123], 1, s[26:27]
	v_cmp_lt_u32_e64 s[14:15], v1, v151
	v_cndmask_b32_e64 v122, 0, v112, s[12:13]
	v_lshl_add_u64 v[152:153], v[122:123], 1, s[26:27]
	v_add_u32_e32 v122, v113, v1
	ds_read2_b32 v[112:113], v169 offset0:140 offset1:145
	ds_read2_b32 v[154:155], v170 offset0:140 offset1:145
	v_cndmask_b32_e64 v122, 0, v122, s[14:15]
	v_lshl_add_u64 v[150:151], v[122:123], 1, s[26:27]
	ds_read2_b32 v[176:177], v169 offset0:150 offset1:155
	ds_read2_b32 v[178:179], v170 offset0:150 offset1:155
	s_waitcnt lgkmcnt(3)
	v_add_u32_e32 v112, v112, v1
	s_waitcnt lgkmcnt(2)
	v_cmp_lt_u32_e64 s[10:11], v1, v154
	v_cmp_lt_u32_e64 s[4:5], v1, v155
	s_waitcnt lgkmcnt(0)
	v_cmp_lt_u32_e64 s[6:7], v1, v178
	v_cndmask_b32_e64 v122, 0, v112, s[10:11]
	v_add_u32_e32 v112, v113, v1
	v_lshl_add_u64 v[174:175], v[122:123], 1, s[26:27]
	v_cndmask_b32_e64 v122, 0, v112, s[4:5]
	v_lshl_add_u64 v[112:113], v[122:123], 1, s[26:27]
	global_load_ushort v172, v[124:125], off
	global_load_ushort v161, v[30:31], off
	global_load_ushort v160, v[32:33], off
	global_load_ushort v159, v[110:111], off
	global_load_ushort v157, v[152:153], off
	global_load_ushort v156, v[150:151], off
	global_load_ushort v155, v[174:175], off
	s_nop 0
	global_load_ushort v153, v[112:113], off
	ds_read_b32 v110, v169 offset:640
	ds_read_b32 v111, v170 offset:640
	v_add_u32_e32 v30, v176, v1
	v_cndmask_b32_e64 v122, 0, v30, s[6:7]
	v_add_u32_e32 v32, v177, v1
	v_cmp_lt_u32_e64 s[8:9], v1, v179
	v_lshl_add_u64 v[30:31], v[122:123], 1, s[26:27]
	s_waitcnt lgkmcnt(1)
	v_add_u32_e32 v110, v110, v1
	v_cndmask_b32_e64 v122, 0, v32, s[8:9]
	s_waitcnt lgkmcnt(0)
	v_cmp_lt_u32_e64 s[0:1], v1, v111
	v_lshl_add_u64 v[32:33], v[122:123], 1, s[26:27]
	s_nop 0
	v_cndmask_b32_e64 v122, 0, v110, s[0:1]
	v_lshl_add_u64 v[110:111], v[122:123], 1, s[26:27]
	global_load_ushort v154, v[30:31], off
	global_load_ushort v152, v[32:33], off
	global_load_ushort v151, v[110:111], off
	s_waitcnt vmcnt(42)
	v_cvt_pk_bf16_f32 v30, v134, v135
	v_cvt_pk_bf16_f32 v31, v136, v137
	s_waitcnt vmcnt(41)
	v_cvt_pk_bf16_f32 v32, v130, v131
	v_cvt_pk_bf16_f32 v33, v132, v133
	ds_write2st64_b64 v171, v[30:31], v[32:33] offset1:1
	s_waitcnt vmcnt(40)
	v_cvt_pk_bf16_f32 v30, v102, v103
	v_cvt_pk_bf16_f32 v31, v104, v105
	s_waitcnt vmcnt(39)
	v_cvt_pk_bf16_f32 v32, v90, v91
	v_cvt_pk_bf16_f32 v33, v92, v93
	ds_write2_b64 v171, v[30:31], v[32:33] offset0:130 offset1:194
	s_waitcnt vmcnt(28)
	v_cvt_pk_bf16_f32 v30, v146, v147
	v_cvt_pk_bf16_f32 v31, v148, v149
	v_cvt_pk_bf16_f32 v32, v118, v119
	v_cvt_pk_bf16_f32 v33, v120, v121
	v_add_u32_e32 v90, 32, v171
	ds_write2st64_b64 v90, v[30:31], v[32:33] offset0:4 offset1:5
	v_cvt_pk_bf16_f32 v30, v78, v79
	v_cvt_pk_bf16_f32 v31, v80, v81
	v_cvt_pk_bf16_f32 v32, v126, v127
	v_cvt_pk_bf16_f32 v33, v128, v129
	v_add_u32_e32 v78, 48, v171
	ds_write2st64_b64 v78, v[30:31], v[32:33] offset0:6 offset1:7
	v_cvt_pk_bf16_f32 v30, v74, v75
	v_cvt_pk_bf16_f32 v31, v76, v77
	v_cvt_pk_bf16_f32 v32, v62, v63
	v_cvt_pk_bf16_f32 v33, v64, v65
	v_add_u32_e32 v62, 64, v171
	ds_write2st64_b64 v62, v[30:31], v[32:33] offset0:8 offset1:9
	v_cvt_pk_bf16_f32 v30, v58, v59
	v_cvt_pk_bf16_f32 v31, v60, v61
	v_cvt_pk_bf16_f32 v32, v46, v47
	v_cvt_pk_bf16_f32 v33, v48, v49
	v_add_u32_e32 v46, 0x50, v171
	ds_write2st64_b64 v46, v[30:31], v[32:33] offset0:10 offset1:11
	v_cvt_pk_bf16_f32 v30, v54, v55
	v_cvt_pk_bf16_f32 v31, v56, v57
	v_cvt_pk_bf16_f32 v32, v42, v43
	v_cvt_pk_bf16_f32 v33, v44, v45
	v_add_u32_e32 v42, 0x60, v171
	v_cvt_pk_bf16_f32 v22, v22, v23
	v_cvt_pk_bf16_f32 v23, v24, v25
	s_waitcnt vmcnt(27)
	v_cvt_pk_bf16_f32 v18, v18, v19
	v_cvt_pk_bf16_f32 v19, v20, v21
	v_add_u32_e32 v20, 0x70, v171
	ds_write2st64_b64 v42, v[30:31], v[32:33] offset0:12 offset1:13
	ds_write2st64_b64 v20, v[22:23], v[18:19] offset0:14 offset1:15
	v_mov_b32_e32 v18, 0xa0
	v_lshl_add_u32 v150, v164, 4, v18
	v_add_u32_e32 v18, s33, v150
	v_min_i32_e32 v18, 0x18698, v18
	v_ashrrev_i32_e32 v19, 31, v18
	v_lshlrev_b64 v[18:19], 11, v[18:19]
	v_lshl_add_u64 v[18:19], v[162:163], 0, v[18:19]
	v_add_co_u32_e64 v20, s[22:23], s34, v18
	global_load_dwordx4 v[134:137], v[18:19], off nt
	global_load_dwordx4 v[126:129], v[18:19], off offset:1024 nt
	global_load_dwordx4 v[110:113], v[18:19], off offset:2048 nt
	global_load_dwordx4 v[102:105], v[18:19], off offset:3072 nt
	v_addc_co_u32_e64 v21, s[22:23], 0, v19, s[22:23]
	v_add_co_u32_e64 v22, s[22:23], s35, v18
	s_nop 1
	v_addc_co_u32_e64 v23, s[22:23], 0, v19, s[22:23]
	v_add_co_u32_e64 v18, s[22:23], s36, v18
	global_load_dwordx4 v[118:121], v[20:21], off offset:1024 nt
	global_load_dwordx4 v[90:93], v[20:21], off offset:2048 nt
	global_load_dwordx4 v[78:81], v[22:23], off nt
	global_load_dwordx4 v[74:77], v[22:23], off offset:1024 nt
	global_load_dwordx4 v[62:65], v[22:23], off offset:2048 nt
	global_load_dwordx4 v[54:57], v[22:23], off offset:3072 nt
	v_addc_co_u32_e64 v19, s[22:23], 0, v19, s[22:23]
	global_load_dwordx4 v[122:125], v[20:21], off offset:3072 nt
	global_load_dwordx4 v[58:61], v[18:19], off nt
	global_load_dwordx4 v[46:49], v[18:19], off offset:1024 nt
	global_load_dwordx4 v[30:33], v[18:19], off offset:2048 nt
	global_load_dwordx4 v[146:149], v[22:23], off offset:-4096 nt
	s_nop 0
	global_load_dwordx4 v[22:25], v[18:19], off offset:3072 nt
	s_waitcnt vmcnt(42)
	v_cvt_pk_bf16_f32 v18, v138, v139
	v_cvt_pk_bf16_f32 v19, v140, v141
	s_waitcnt vmcnt(41)
	v_cvt_pk_bf16_f32 v20, v114, v115
	v_cvt_pk_bf16_f32 v21, v116, v117
	v_add_u32_e32 v42, 0x80, v171
	ds_write2st64_b64 v42, v[18:19], v[20:21] offset0:16 offset1:17
	s_waitcnt vmcnt(40)
	v_cvt_pk_bf16_f32 v18, v106, v107
	v_cvt_pk_bf16_f32 v19, v108, v109
	s_waitcnt vmcnt(39)
	v_cvt_pk_bf16_f32 v20, v94, v95
	v_cvt_pk_bf16_f32 v21, v96, v97
	v_add_u32_e32 v42, 0x90, v171
	ds_write2st64_b64 v42, v[18:19], v[20:21] offset0:18 offset1:19
	s_waitcnt vmcnt(28)
	v_cvt_pk_bf16_f32 v18, v142, v143
	v_cvt_pk_bf16_f32 v19, v144, v145
	v_cvt_pk_bf16_f32 v20, v98, v99
	v_cvt_pk_bf16_f32 v21, v100, v101
	v_add_u32_e32 v42, 0xa0, v171
	ds_write2st64_b64 v42, v[18:19], v[20:21] offset0:20 offset1:21
	v_cvt_pk_bf16_f32 v18, v82, v83
	v_cvt_pk_bf16_f32 v19, v84, v85
	v_cvt_pk_bf16_f32 v20, v86, v87
	v_cvt_pk_bf16_f32 v21, v88, v89
	v_add_u32_e32 v42, 0xb0, v171
	ds_write2st64_b64 v42, v[18:19], v[20:21] offset0:22 offset1:23
	v_cvt_pk_bf16_f32 v18, v70, v71
	v_cvt_pk_bf16_f32 v19, v72, v73
	v_cvt_pk_bf16_f32 v20, v66, v67
	v_cvt_pk_bf16_f32 v21, v68, v69
	v_add_u32_e32 v42, 0xc0, v171
	ds_write2st64_b64 v42, v[18:19], v[20:21] offset0:24 offset1:25
	v_cvt_pk_bf16_f32 v18, v50, v51
	v_cvt_pk_bf16_f32 v19, v52, v53
	v_cvt_pk_bf16_f32 v20, v34, v35
	v_cvt_pk_bf16_f32 v21, v36, v37
	v_add_u32_e32 v34, 0xd0, v171
	ds_write2st64_b64 v34, v[18:19], v[20:21] offset0:26 offset1:27
	v_cvt_pk_bf16_f32 v18, v38, v39
	v_cvt_pk_bf16_f32 v19, v40, v41
	v_cvt_pk_bf16_f32 v20, v26, v27
	v_cvt_pk_bf16_f32 v21, v28, v29
	v_add_u32_e32 v26, 0xe0, v171
	v_cvt_pk_bf16_f32 v14, v14, v15
	v_cvt_pk_bf16_f32 v15, v16, v17
	s_waitcnt vmcnt(27)
	v_cvt_pk_bf16_f32 v10, v10, v11
	v_cvt_pk_bf16_f32 v11, v12, v13
	v_add_u32_e32 v12, 0xf0, v171
	ds_write2st64_b64 v26, v[18:19], v[20:21] offset0:28 offset1:29
	ds_write2st64_b64 v12, v[14:15], v[10:11] offset0:30 offset1:31
	v_add_u32_e32 v10, s31, v150
	v_min_i32_e32 v10, 0x18698, v10
	v_ashrrev_i32_e32 v11, 31, v10
	v_lshlrev_b64 v[10:11], 11, v[10:11]
	v_lshl_add_u64 v[10:11], v[162:163], 0, v[10:11]
	v_add_co_u32_e64 v12, s[22:23], s34, v10
	global_load_dwordx4 v[138:141], v[10:11], off nt
	global_load_dwordx4 v[130:133], v[10:11], off offset:1024 nt
	global_load_dwordx4 v[114:117], v[10:11], off offset:2048 nt
	global_load_dwordx4 v[94:97], v[10:11], off offset:3072 nt
	v_addc_co_u32_e64 v13, s[22:23], 0, v11, s[22:23]
	v_add_co_u32_e64 v14, s[22:23], s35, v10
	s_nop 1
	v_addc_co_u32_e64 v15, s[22:23], 0, v11, s[22:23]
	v_add_co_u32_e64 v10, s[22:23], s36, v10
	global_load_dwordx4 v[98:101], v[12:13], off offset:1024 nt
	global_load_dwordx4 v[82:85], v[12:13], off offset:2048 nt
	global_load_dwordx4 v[70:73], v[14:15], off nt
	global_load_dwordx4 v[66:69], v[14:15], off offset:1024 nt
	global_load_dwordx4 v[50:53], v[14:15], off offset:2048 nt
	global_load_dwordx4 v[38:41], v[14:15], off offset:3072 nt
	v_addc_co_u32_e64 v11, s[22:23], 0, v11, s[22:23]
	global_load_dwordx4 v[86:89], v[12:13], off offset:3072 nt
	global_load_dwordx4 v[42:45], v[10:11], off nt
	global_load_dwordx4 v[34:37], v[10:11], off offset:1024 nt
	global_load_dwordx4 v[18:21], v[10:11], off offset:2048 nt
	global_load_dwordx4 v[142:145], v[14:15], off offset:-4096 nt
	s_nop 0
	global_load_dwordx4 v[14:17], v[10:11], off offset:3072 nt
	v_mov_b32_e32 v10, 0x14500
	v_lshl_add_u32 v173, v173, 4, v10
	ds_read_b128 v[10:13], v173
	ds_read_b128 v[26:29], v173 offset:1024
	ds_read_b128 v[106:109], v168
	ds_read_b128 v[174:177], v168 offset:16
	s_waitcnt lgkmcnt(1)
	v_mfma_f32_16x16x32_bf16 v[10:13], v[10:13], v[106:109], 0
	ds_read_b128 v[106:109], v173 offset:2048
	ds_read_b128 v[178:181], v173 offset:3072
	s_waitcnt lgkmcnt(2)
	v_mfma_f32_16x16x32_bf16 v[10:13], v[26:29], v[174:177], v[10:13]
	ds_read_b128 v[26:29], v168 offset:32
	ds_read_b128 v[174:177], v168 offset:48
	s_waitcnt lgkmcnt(1)
	v_mfma_f32_16x16x32_bf16 v[10:13], v[106:109], v[26:29], v[10:13]
	s_waitcnt lgkmcnt(0)
	v_mfma_f32_16x16x32_bf16 v[10:13], v[178:181], v[174:177], v[10:13]
	ds_read_b128 v[26:29], v173 offset:4096
	ds_read_b128 v[106:109], v173 offset:5120
	ds_read_b128 v[174:177], v168 offset:64
	ds_read_b128 v[178:181], v168 offset:80
	s_waitcnt lgkmcnt(1)
	v_mfma_f32_16x16x32_bf16 v[10:13], v[26:29], v[174:177], v[10:13]
	ds_read_b128 v[26:29], v173 offset:6144
	ds_read_b128 v[174:177], v173 offset:7168
	s_waitcnt lgkmcnt(2)
	v_mfma_f32_16x16x32_bf16 v[10:13], v[106:109], v[178:181], v[10:13]
	ds_read_b128 v[106:109], v168 offset:96
	ds_read_b128 v[178:181], v168 offset:112
	s_waitcnt lgkmcnt(1)
	v_mfma_f32_16x16x32_bf16 v[10:13], v[26:29], v[106:109], v[10:13]
	s_waitcnt lgkmcnt(0)
	v_mfma_f32_16x16x32_bf16 v[10:13], v[174:177], v[178:181], v[10:13]
	ds_read_b128 v[26:29], v173 offset:8192
	ds_read_b128 v[106:109], v173 offset:9216
	ds_read_b128 v[174:177], v168 offset:128
	ds_read_b128 v[178:181], v168 offset:144
	s_waitcnt lgkmcnt(1)
	v_mfma_f32_16x16x32_bf16 v[10:13], v[26:29], v[174:177], v[10:13]
	ds_read_b128 v[26:29], v173 offset:10240
	ds_read_b128 v[174:177], v173 offset:11264
	s_waitcnt lgkmcnt(2)
	v_mfma_f32_16x16x32_bf16 v[10:13], v[106:109], v[178:181], v[10:13]
	ds_read_b128 v[106:109], v168 offset:160
	ds_read_b128 v[178:181], v168 offset:176
	s_waitcnt lgkmcnt(1)
	v_mfma_f32_16x16x32_bf16 v[10:13], v[26:29], v[106:109], v[10:13]
	s_waitcnt lgkmcnt(0)
	v_mfma_f32_16x16x32_bf16 v[10:13], v[174:177], v[178:181], v[10:13]
	ds_read_b128 v[26:29], v173 offset:12288
	ds_read_b128 v[106:109], v173 offset:13312
	ds_read_b128 v[174:177], v168 offset:192
	ds_read_b128 v[178:181], v168 offset:208
	s_waitcnt lgkmcnt(1)
	v_mfma_f32_16x16x32_bf16 v[10:13], v[26:29], v[174:177], v[10:13]
	ds_read_b128 v[26:29], v173 offset:14336
	ds_read_b128 v[174:177], v173 offset:15360
	s_waitcnt lgkmcnt(2)
	v_mfma_f32_16x16x32_bf16 v[10:13], v[106:109], v[178:181], v[10:13]
	ds_read_b128 v[106:109], v168 offset:224
	ds_read_b128 v[178:181], v168 offset:240
	s_waitcnt lgkmcnt(1)
	v_mfma_f32_16x16x32_bf16 v[10:13], v[26:29], v[106:109], v[10:13]
	s_waitcnt lgkmcnt(0)
	v_mfma_f32_16x16x32_bf16 v[10:13], v[174:177], v[178:181], v[10:13]
	s_waitcnt vmcnt(42)
	v_cmp_ne_u16_e64 s[22:23], -1, v172
	s_and_b64 s[22:23], s[20:21], s[22:23]
	s_and_saveexec_b64 s[20:21], s[22:23]
	v_and_b32_e32 v26, 0xffff, v172
	v_mov_b32_e32 v27, 0x18500
	v_lshl_add_u32 v26, v26, 2, v27
	v_mov_b32_e32 v27, 1
	ds_add_u32 v26, v27
	s_or_b64 exec, exec, s[20:21]
	v_mov_b32_e32 v26, 0xffff
	s_mov_b32 s22, 0xffff
	s_waitcnt vmcnt(41)
	v_cndmask_b32_sdwa v27, v26, v161, vcc dst_sel:DWORD dst_unused:UNUSED_PAD src0_sel:DWORD src1_sel:WORD_0
	v_cmp_ne_u32_e32 vcc, s22, v27
	s_and_saveexec_b64 s[20:21], vcc
	v_mov_b32_e32 v28, 0x18500
	v_lshl_add_u32 v27, v27, 2, v28
	v_mov_b32_e32 v28, 1
	ds_add_u32 v27, v28
	s_or_b64 exec, exec, s[20:21]
	s_mov_b64 vcc, s[16:17]
	s_waitcnt vmcnt(40)
	v_cndmask_b32_sdwa v26, v26, v160, vcc dst_sel:DWORD dst_unused:UNUSED_PAD src0_sel:DWORD src1_sel:WORD_0
	v_cmp_ne_u32_e32 vcc, s22, v26
	s_and_saveexec_b64 s[16:17], vcc
	v_mov_b32_e32 v27, 0x18500
	v_lshl_add_u32 v26, v26, 2, v27
	v_mov_b32_e32 v27, 1
	ds_add_u32 v26, v27
	s_or_b64 exec, exec, s[16:17]
	s_mov_b64 vcc, s[18:19]
	v_mov_b32_e32 v26, 0xffff
	s_mov_b32 s18, 0xffff
	s_waitcnt vmcnt(39)
	v_cndmask_b32_sdwa v27, v26, v159, vcc dst_sel:DWORD dst_unused:UNUSED_PAD src0_sel:DWORD src1_sel:WORD_0
	v_cmp_ne_u32_e32 vcc, s18, v27
	s_and_saveexec_b64 s[16:17], vcc
	v_mov_b32_e32 v28, 0x18500
	v_lshl_add_u32 v27, v27, 2, v28
	v_mov_b32_e32 v28, 1
	ds_add_u32 v27, v28
	s_or_b64 exec, exec, s[16:17]
	s_mov_b64 vcc, s[12:13]
	s_waitcnt vmcnt(38)
	v_cndmask_b32_sdwa v26, v26, v157, vcc dst_sel:DWORD dst_unused:UNUSED_PAD src0_sel:DWORD src1_sel:WORD_0
	v_cmp_ne_u32_e32 vcc, s18, v26
	s_and_saveexec_b64 s[12:13], vcc
	v_mov_b32_e32 v27, 0x18500
	v_lshl_add_u32 v26, v26, 2, v27
	v_mov_b32_e32 v27, 1
	ds_add_u32 v26, v27
	s_or_b64 exec, exec, s[12:13]
	s_mov_b64 vcc, s[14:15]
	v_mov_b32_e32 v26, 0xffff
	s_mov_b32 s14, 0xffff
	s_waitcnt vmcnt(37)
	v_cndmask_b32_sdwa v27, v26, v156, vcc dst_sel:DWORD dst_unused:UNUSED_PAD src0_sel:DWORD src1_sel:WORD_0
	v_cmp_ne_u32_e32 vcc, s14, v27
	s_and_saveexec_b64 s[12:13], vcc
	v_mov_b32_e32 v28, 0x18500
	v_lshl_add_u32 v27, v27, 2, v28
	v_mov_b32_e32 v28, 1
	ds_add_u32 v27, v28
	s_or_b64 exec, exec, s[12:13]
	s_mov_b64 vcc, s[10:11]
	s_waitcnt vmcnt(36)
	v_cndmask_b32_sdwa v26, v26, v155, vcc dst_sel:DWORD dst_unused:UNUSED_PAD src0_sel:DWORD src1_sel:WORD_0
	v_cmp_ne_u32_e32 vcc, s14, v26
	s_and_saveexec_b64 s[10:11], vcc
	v_mov_b32_e32 v27, 0x18500
	v_lshl_add_u32 v26, v26, 2, v27
	v_mov_b32_e32 v27, 1
	ds_add_u32 v26, v27
	s_or_b64 exec, exec, s[10:11]
	s_mov_b64 vcc, s[4:5]
	v_mov_b32_e32 v26, 0xffff
	s_mov_b32 s10, 0xffff
	s_waitcnt vmcnt(35)
	v_cndmask_b32_sdwa v27, v26, v153, vcc dst_sel:DWORD dst_unused:UNUSED_PAD src0_sel:DWORD src1_sel:WORD_0
	v_cmp_ne_u32_e32 vcc, s10, v27
	s_and_saveexec_b64 s[4:5], vcc
	v_mov_b32_e32 v28, 0x18500
	v_lshl_add_u32 v27, v27, 2, v28
	v_mov_b32_e32 v28, 1
	ds_add_u32 v27, v28
	s_or_b64 exec, exec, s[4:5]
	s_mov_b64 vcc, s[6:7]
	s_waitcnt vmcnt(34)
	v_cndmask_b32_sdwa v26, v26, v154, vcc dst_sel:DWORD dst_unused:UNUSED_PAD src0_sel:DWORD src1_sel:WORD_0
	v_cmp_ne_u32_e32 vcc, s10, v26
	s_and_saveexec_b64 s[4:5], vcc
	v_mov_b32_e32 v27, 0x18500
	v_lshl_add_u32 v26, v26, 2, v27
	v_mov_b32_e32 v27, 1
	ds_add_u32 v26, v27
	s_or_b64 exec, exec, s[4:5]
	s_mov_b64 vcc, s[8:9]
	v_mov_b32_e32 v26, 0xffff
	s_mov_b32 s6, 0xffff
	s_waitcnt vmcnt(33)
	v_cndmask_b32_sdwa v27, v26, v152, vcc dst_sel:DWORD dst_unused:UNUSED_PAD src0_sel:DWORD src1_sel:WORD_0
	v_cmp_ne_u32_e32 vcc, s6, v27
	s_and_saveexec_b64 s[4:5], vcc
	v_mov_b32_e32 v28, 0x18500
	v_lshl_add_u32 v27, v27, 2, v28
	v_mov_b32_e32 v28, 1
	ds_add_u32 v27, v28
	s_or_b64 exec, exec, s[4:5]
	s_mov_b64 vcc, s[0:1]
	s_waitcnt vmcnt(32)
	v_cndmask_b32_sdwa v26, v26, v151, vcc dst_sel:DWORD dst_unused:UNUSED_PAD src0_sel:DWORD src1_sel:WORD_0
	v_cmp_ne_u32_e32 vcc, s6, v26
	s_and_saveexec_b64 s[0:1], vcc
	v_mov_b32_e32 v27, 0x18500
	v_lshl_add_u32 v26, v26, 2, v27
	v_mov_b32_e32 v27, 1
	ds_add_u32 v26, v27
	s_or_b64 exec, exec, s[0:1]
	v_mov_b32_e32 v173, v1
	ds_read2_b32 v[26:27], v169 offset0:165 offset1:170
	ds_read2_b32 v[28:29], v170 offset0:165 offset1:170
	ds_read2_b32 v[106:107], v170 offset0:175 offset1:180
	ds_read2_b32 v[108:109], v169 offset0:175 offset1:180
	v_mov_b32_e32 v175, 0
	s_waitcnt lgkmcnt(3)
	v_add_u32_e32 v26, v26, v1
	s_waitcnt lgkmcnt(2)
	v_cmp_lt_u32_e64 s[20:21], v1, v28
	s_waitcnt lgkmcnt(1)
	v_cmp_lt_u32_e64 s[16:17], v1, v106
	s_waitcnt lgkmcnt(0)
	v_add_u32_e32 v28, v108, v1
	v_add_u32_e32 v106, v109, v1
	ds_read2_b32 v[108:109], v169 offset0:185 offset1:190
	ds_read2_b32 v[154:155], v170 offset0:185 offset1:190
	v_cndmask_b32_e64 v174, 0, v26, s[20:21]
	v_add_u32_e32 v26, v27, v1
	v_cmp_lt_u32_e32 vcc, v1, v29
	v_lshl_add_u64 v[152:153], v[174:175], 1, s[26:27]
	v_cmp_lt_u32_e64 s[18:19], v1, v107
	v_cndmask_b32_e32 v174, 0, v26, vcc
	v_lshl_add_u64 v[26:27], v[174:175], 1, s[26:27]
	v_cndmask_b32_e64 v174, 0, v28, s[16:17]
	v_lshl_add_u64 v[28:29], v[174:175], 1, s[26:27]
	v_cndmask_b32_e64 v174, 0, v106, s[18:19]
	s_waitcnt lgkmcnt(1)
	v_add_u32_e32 v108, v108, v1
	s_waitcnt lgkmcnt(0)
	v_cmp_lt_u32_e64 s[12:13], v1, v154
	v_lshl_add_u64 v[106:107], v[174:175], 1, s[26:27]
	v_add_u32_e32 v151, v109, v1
	v_cndmask_b32_e64 v174, 0, v108, s[12:13]
	ds_read2_b32 v[108:109], v169 offset0:195 offset1:200
	ds_read2_b32 v[160:161], v170 offset0:195 offset1:200
	v_cmp_lt_u32_e64 s[14:15], v1, v155
	v_lshl_add_u64 v[156:157], v[174:175], 1, s[26:27]
	ds_read2_b32 v[178:179], v169 offset0:205 offset1:210
	ds_read2_b32 v[180:181], v170 offset0:205 offset1:210
	v_cndmask_b32_e64 v174, 0, v151, s[14:15]
	s_waitcnt lgkmcnt(3)
	v_add_u32_e32 v108, v108, v1
	s_waitcnt lgkmcnt(2)
	v_cmp_lt_u32_e64 s[10:11], v1, v160
	v_lshl_add_u64 v[154:155], v[174:175], 1, s[26:27]
	v_cmp_lt_u32_e64 s[4:5], v1, v161
	v_cndmask_b32_e64 v174, 0, v108, s[10:11]
	v_add_u32_e32 v108, v109, v1
	v_lshl_add_u64 v[176:177], v[174:175], 1, s[26:27]
	v_cndmask_b32_e64 v174, 0, v108, s[4:5]
	v_lshl_add_u64 v[108:109], v[174:175], 1, s[26:27]
	global_load_ushort v172, v[152:153], off
	global_load_ushort v161, v[26:27], off
	global_load_ushort v160, v[28:29], off
	global_load_ushort v159, v[106:107], off
	s_nop 0
	global_load_ushort v157, v[156:157], off
	s_nop 0
	global_load_ushort v156, v[154:155], off
	s_nop 0
	global_load_ushort v155, v[176:177], off
	global_load_ushort v153, v[108:109], off
	ds_read_b32 v106, v169 offset:860
	ds_read_b32 v107, v170 offset:860
	s_waitcnt lgkmcnt(3)
	v_add_u32_e32 v26, v178, v1
	s_waitcnt lgkmcnt(2)
	v_cmp_lt_u32_e64 s[6:7], v1, v180
	v_add_u32_e32 v28, v179, v1
	v_cmp_lt_u32_e64 s[8:9], v1, v181
	v_cndmask_b32_e64 v174, 0, v26, s[6:7]
	v_lshl_add_u64 v[26:27], v[174:175], 1, s[26:27]
	v_cndmask_b32_e64 v174, 0, v28, s[8:9]
	s_waitcnt lgkmcnt(1)
	v_add_u32_e32 v106, v106, v1
	s_waitcnt lgkmcnt(0)
	v_cmp_lt_u32_e64 s[0:1], v1, v107
	v_lshl_add_u64 v[28:29], v[174:175], 1, s[26:27]
	s_nop 0
	v_cndmask_b32_e64 v174, 0, v106, s[0:1]
	v_lshl_add_u64 v[106:107], v[174:175], 1, s[26:27]
	global_load_ushort v154, v[26:27], off
	global_load_ushort v152, v[28:29], off
	global_load_ushort v151, v[106:107], off
	s_waitcnt vmcnt(42)
	v_cvt_pk_bf16_f32 v26, v134, v135
	v_cvt_pk_bf16_f32 v27, v136, v137
	s_waitcnt vmcnt(41)
	v_cvt_pk_bf16_f32 v28, v126, v127
	v_cvt_pk_bf16_f32 v29, v128, v129
	ds_write2st64_b64 v171, v[26:27], v[28:29] offset1:1
	s_waitcnt vmcnt(40)
	v_cvt_pk_bf16_f32 v26, v110, v111
	v_cvt_pk_bf16_f32 v27, v112, v113
	s_waitcnt vmcnt(39)
	v_cvt_pk_bf16_f32 v28, v102, v103
	v_cvt_pk_bf16_f32 v29, v104, v105
	ds_write2_b64 v171, v[26:27], v[28:29] offset0:130 offset1:194
	s_waitcnt vmcnt(28)
	v_cvt_pk_bf16_f32 v26, v146, v147
	v_cvt_pk_bf16_f32 v27, v148, v149
	v_cvt_pk_bf16_f32 v28, v118, v119
	v_cvt_pk_bf16_f32 v29, v120, v121
	v_add_u32_e32 v102, 32, v171
	ds_write2st64_b64 v102, v[26:27], v[28:29] offset0:4 offset1:5
	v_cvt_pk_bf16_f32 v26, v90, v91
	v_cvt_pk_bf16_f32 v27, v92, v93
	v_cvt_pk_bf16_f32 v28, v122, v123
	v_cvt_pk_bf16_f32 v29, v124, v125
	v_add_u32_e32 v90, 48, v171
	ds_write2st64_b64 v90, v[26:27], v[28:29] offset0:6 offset1:7
	v_cvt_pk_bf16_f32 v26, v78, v79
	v_cvt_pk_bf16_f32 v27, v80, v81
	v_cvt_pk_bf16_f32 v28, v74, v75
	v_cvt_pk_bf16_f32 v29, v76, v77
	v_add_u32_e32 v74, 64, v171
	ds_write2st64_b64 v74, v[26:27], v[28:29] offset0:8 offset1:9
	v_cvt_pk_bf16_f32 v26, v62, v63
	v_cvt_pk_bf16_f32 v27, v64, v65
	v_cvt_pk_bf16_f32 v28, v54, v55
	v_cvt_pk_bf16_f32 v29, v56, v57
	v_add_u32_e32 v54, 0x50, v171
	ds_write2st64_b64 v54, v[26:27], v[28:29] offset0:10 offset1:11
	v_cvt_pk_bf16_f32 v26, v58, v59
	v_cvt_pk_bf16_f32 v27, v60, v61
	v_cvt_pk_bf16_f32 v28, v46, v47
	v_cvt_pk_bf16_f32 v29, v48, v49
	v_add_u32_e32 v46, 0x60, v171
	ds_write2st64_b64 v46, v[26:27], v[28:29] offset0:12 offset1:13
	v_cvt_pk_bf16_f32 v26, v30, v31
	v_cvt_pk_bf16_f32 v27, v32, v33
	s_waitcnt vmcnt(27)
	v_cvt_pk_bf16_f32 v22, v22, v23
	v_cvt_pk_bf16_f32 v23, v24, v25
	v_add_u32_e32 v24, 0x70, v171
	ds_write2st64_b64 v24, v[26:27], v[22:23] offset0:14 offset1:15
	v_mov_b32_e32 v22, 0xf0
	v_lshl_add_u32 v146, v164, 4, v22
	v_add_u32_e32 v22, s33, v146
	v_min_i32_e32 v22, 0x18698, v22
	v_ashrrev_i32_e32 v23, 31, v22
	v_lshlrev_b64 v[22:23], 11, v[22:23]
	v_lshl_add_u64 v[22:23], v[162:163], 0, v[22:23]
	s_movk_i32 s33, 0x1000
	v_add_co_u32_e64 v24, s[22:23], s33, v22
	s_movk_i32 s34, 0x2000
	s_nop 0
	v_addc_co_u32_e64 v25, s[22:23], 0, v23, s[22:23]
	v_add_co_u32_e64 v126, s[22:23], s34, v22
	s_movk_i32 s35, 0x3000
	s_nop 0
	v_addc_co_u32_e64 v127, s[22:23], 0, v23, s[22:23]
	global_load_dwordx4 v[122:125], v[22:23], off nt
	global_load_dwordx4 v[118:121], v[22:23], off offset:1024 nt
	global_load_dwordx4 v[102:105], v[22:23], off offset:2048 nt
	global_load_dwordx4 v[90:93], v[22:23], off offset:3072 nt
	v_add_co_u32_e64 v22, s[22:23], s35, v22
	global_load_dwordx4 v[106:109], v[24:25], off offset:1024 nt
	global_load_dwordx4 v[78:81], v[24:25], off offset:2048 nt
	global_load_dwordx4 v[74:77], v[126:127], off nt
	global_load_dwordx4 v[62:65], v[126:127], off offset:1024 nt
	global_load_dwordx4 v[58:61], v[126:127], off offset:2048 nt
	global_load_dwordx4 v[46:49], v[126:127], off offset:3072 nt
	v_addc_co_u32_e64 v23, s[22:23], 0, v23, s[22:23]
	global_load_dwordx4 v[110:113], v[24:25], off offset:3072 nt
	global_load_dwordx4 v[54:57], v[22:23], off nt
	global_load_dwordx4 v[30:33], v[22:23], off offset:1024 nt
	global_load_dwordx4 v[26:29], v[22:23], off offset:2048 nt
	s_nop 0
	global_load_dwordx4 v[126:129], v[126:127], off offset:-4096 nt
	s_nop 0
	global_load_dwordx4 v[22:25], v[22:23], off offset:3072 nt
	s_waitcnt vmcnt(40)
	v_cvt_pk_bf16_f32 v114, v114, v115
	v_cvt_pk_bf16_f32 v115, v116, v117
	s_waitcnt vmcnt(39)
	v_cvt_pk_bf16_f32 v94, v94, v95
	v_cvt_pk_bf16_f32 v95, v96, v97
	v_add_u32_e32 v96, 0x90, v171
	s_waitcnt vmcnt(34)
	v_cvt_pk_bf16_f32 v50, v50, v51
	v_cvt_pk_bf16_f32 v51, v52, v53
	s_waitcnt vmcnt(33)
	v_cvt_pk_bf16_f32 v38, v38, v39
	v_cvt_pk_bf16_f32 v39, v40, v41
	v_add_u32_e32 v40, 0xd0, v171
	v_cvt_pk_bf16_f32 v134, v138, v139
	v_cvt_pk_bf16_f32 v135, v140, v141
	v_cvt_pk_bf16_f32 v130, v130, v131
	v_cvt_pk_bf16_f32 v131, v132, v133
	v_add_u32_e32 v132, 0x80, v171
	ds_write2st64_b64 v96, v[114:115], v[94:95] offset0:18 offset1:19
	s_waitcnt vmcnt(28)
	v_cvt_pk_bf16_f32 v94, v142, v143
	v_cvt_pk_bf16_f32 v95, v144, v145
	v_cvt_pk_bf16_f32 v96, v98, v99
	v_cvt_pk_bf16_f32 v97, v100, v101
	v_add_u32_e32 v98, 0xa0, v171
	v_cvt_pk_bf16_f32 v82, v82, v83
	v_cvt_pk_bf16_f32 v83, v84, v85
	v_cvt_pk_bf16_f32 v84, v86, v87
	v_cvt_pk_bf16_f32 v85, v88, v89
	v_add_u32_e32 v86, 0xb0, v171
	v_cvt_pk_bf16_f32 v70, v70, v71
	v_cvt_pk_bf16_f32 v71, v72, v73
	v_cvt_pk_bf16_f32 v66, v66, v67
	v_cvt_pk_bf16_f32 v67, v68, v69
	v_add_u32_e32 v68, 0xc0, v171
	ds_write2st64_b64 v40, v[50:51], v[38:39] offset0:26 offset1:27
	v_cvt_pk_bf16_f32 v38, v42, v43
	v_cvt_pk_bf16_f32 v39, v44, v45
	v_cvt_pk_bf16_f32 v34, v34, v35
	v_cvt_pk_bf16_f32 v35, v36, v37
	v_add_u32_e32 v36, 0xe0, v171
	v_cvt_pk_bf16_f32 v18, v18, v19
	v_cvt_pk_bf16_f32 v19, v20, v21
	s_waitcnt vmcnt(27)
	v_cvt_pk_bf16_f32 v14, v14, v15
	v_cvt_pk_bf16_f32 v15, v16, v17
	v_add_u32_e32 v16, 0xf0, v171
	ds_write2st64_b64 v132, v[134:135], v[130:131] offset0:16 offset1:17
	ds_write2st64_b64 v98, v[94:95], v[96:97] offset0:20 offset1:21
	ds_write2st64_b64 v86, v[82:83], v[84:85] offset0:22 offset1:23
	ds_write2st64_b64 v68, v[70:71], v[66:67] offset0:24 offset1:25
	ds_write2st64_b64 v36, v[38:39], v[34:35] offset0:28 offset1:29
	ds_write2st64_b64 v16, v[18:19], v[14:15] offset0:30 offset1:31
	v_add_u32_e32 v14, s31, v146
	v_min_i32_e32 v14, 0x18698, v14
	v_ashrrev_i32_e32 v15, 31, v14
	v_lshlrev_b64 v[14:15], 11, v[14:15]
	v_lshl_add_u64 v[14:15], v[162:163], 0, v[14:15]
	v_add_co_u32_e64 v16, s[22:23], s33, v14
	global_load_dwordx4 v[138:141], v[14:15], off nt
	global_load_dwordx4 v[134:137], v[14:15], off offset:1024 nt
	global_load_dwordx4 v[130:133], v[14:15], off offset:2048 nt
	global_load_dwordx4 v[98:101], v[14:15], off offset:3072 nt
	v_addc_co_u32_e64 v17, s[22:23], 0, v15, s[22:23]
	v_add_co_u32_e64 v18, s[22:23], s34, v14
	s_nop 1
	v_addc_co_u32_e64 v19, s[22:23], 0, v15, s[22:23]
	v_add_co_u32_e64 v14, s[22:23], s35, v14
	global_load_dwordx4 v[114:117], v[16:17], off offset:1024 nt
	global_load_dwordx4 v[86:89], v[16:17], off offset:2048 nt
	global_load_dwordx4 v[82:85], v[18:19], off nt
	global_load_dwordx4 v[70:73], v[18:19], off offset:1024 nt
	global_load_dwordx4 v[66:69], v[18:19], off offset:2048 nt
	global_load_dwordx4 v[42:45], v[18:19], off offset:3072 nt
	v_addc_co_u32_e64 v15, s[22:23], 0, v15, s[22:23]
	global_load_dwordx4 v[94:97], v[16:17], off offset:3072 nt
	global_load_dwordx4 v[50:53], v[14:15], off nt
	global_load_dwordx4 v[38:41], v[14:15], off offset:1024 nt
	global_load_dwordx4 v[34:37], v[14:15], off offset:2048 nt
	global_load_dwordx4 v[142:145], v[18:19], off offset:-4096 nt
	s_nop 0
	global_load_dwordx4 v[18:21], v[14:15], off offset:3072 nt
	v_mov_b32_e32 v14, 0x14500
	v_lshl_add_u32 v147, v173, 4, v14
	ds_read_b128 v[14:17], v147
	ds_read_b128 v[174:177], v147 offset:1024
	ds_read_b128 v[178:181], v168
	ds_read_b128 v[182:185], v168 offset:16
	s_waitcnt lgkmcnt(1)
	v_mfma_f32_16x16x32_bf16 v[14:17], v[14:17], v[178:181], 0
	ds_read_b128 v[178:181], v147 offset:2048
	ds_read_b128 v[186:189], v147 offset:3072
	s_waitcnt lgkmcnt(2)
	v_mfma_f32_16x16x32_bf16 v[14:17], v[174:177], v[182:185], v[14:17]
	ds_read_b128 v[174:177], v168 offset:32
	ds_read_b128 v[182:185], v168 offset:48
	s_waitcnt lgkmcnt(1)
	v_mfma_f32_16x16x32_bf16 v[14:17], v[178:181], v[174:177], v[14:17]
	s_waitcnt lgkmcnt(0)
	v_mfma_f32_16x16x32_bf16 v[14:17], v[186:189], v[182:185], v[14:17]
	ds_read_b128 v[174:177], v147 offset:4096
	ds_read_b128 v[178:181], v147 offset:5120
	ds_read_b128 v[182:185], v168 offset:64
	ds_read_b128 v[186:189], v168 offset:80
	s_waitcnt lgkmcnt(1)
	v_mfma_f32_16x16x32_bf16 v[14:17], v[174:177], v[182:185], v[14:17]
	ds_read_b128 v[174:177], v147 offset:6144
	ds_read_b128 v[182:185], v147 offset:7168
	s_waitcnt lgkmcnt(2)
	v_mfma_f32_16x16x32_bf16 v[14:17], v[178:181], v[186:189], v[14:17]
	ds_read_b128 v[178:181], v168 offset:96
	ds_read_b128 v[186:189], v168 offset:112
	s_waitcnt lgkmcnt(1)
	v_mfma_f32_16x16x32_bf16 v[14:17], v[174:177], v[178:181], v[14:17]
	s_waitcnt lgkmcnt(0)
	v_mfma_f32_16x16x32_bf16 v[14:17], v[182:185], v[186:189], v[14:17]
	ds_read_b128 v[174:177], v147 offset:8192
	ds_read_b128 v[178:181], v147 offset:9216
	ds_read_b128 v[182:185], v168 offset:128
	ds_read_b128 v[186:189], v168 offset:144
	s_waitcnt lgkmcnt(1)
	v_mfma_f32_16x16x32_bf16 v[14:17], v[174:177], v[182:185], v[14:17]
	ds_read_b128 v[174:177], v147 offset:10240
	ds_read_b128 v[182:185], v147 offset:11264
	s_waitcnt lgkmcnt(2)
	v_mfma_f32_16x16x32_bf16 v[14:17], v[178:181], v[186:189], v[14:17]
	ds_read_b128 v[178:181], v168 offset:160
	ds_read_b128 v[186:189], v168 offset:176
	s_waitcnt lgkmcnt(1)
	v_mfma_f32_16x16x32_bf16 v[14:17], v[174:177], v[178:181], v[14:17]
	s_waitcnt lgkmcnt(0)
	v_mfma_f32_16x16x32_bf16 v[14:17], v[182:185], v[186:189], v[14:17]
	ds_read_b128 v[174:177], v147 offset:12288
	ds_read_b128 v[178:181], v147 offset:13312
	ds_read_b128 v[182:185], v168 offset:192
	ds_read_b128 v[186:189], v168 offset:208
	s_waitcnt lgkmcnt(1)
	v_mfma_f32_16x16x32_bf16 v[14:17], v[174:177], v[182:185], v[14:17]
	ds_read_b128 v[174:177], v147 offset:14336
	ds_read_b128 v[182:185], v147 offset:15360
	s_waitcnt lgkmcnt(2)
	v_mfma_f32_16x16x32_bf16 v[14:17], v[178:181], v[186:189], v[14:17]
	ds_read_b128 v[178:181], v168 offset:224
	ds_read_b128 v[186:189], v168 offset:240
	s_waitcnt lgkmcnt(1)
	v_mfma_f32_16x16x32_bf16 v[14:17], v[174:177], v[178:181], v[14:17]
	s_waitcnt lgkmcnt(0)
	v_mfma_f32_16x16x32_bf16 v[14:17], v[182:185], v[186:189], v[14:17]
	s_waitcnt vmcnt(42)
	v_cmp_ne_u16_e64 s[22:23], -1, v172
	s_and_b64 s[22:23], s[20:21], s[22:23]
	s_and_saveexec_b64 s[20:21], s[22:23]
	v_and_b32_e32 v147, 0xffff, v172
	v_mov_b32_e32 v148, 0x18500
	v_lshl_add_u32 v147, v147, 2, v148
	v_mov_b32_e32 v148, 1
	ds_add_u32 v147, v148
	s_or_b64 exec, exec, s[20:21]
	v_mov_b32_e32 v147, 0xffff
	s_mov_b32 s22, 0xffff
	s_waitcnt vmcnt(41)
	v_cndmask_b32_sdwa v148, v147, v161, vcc dst_sel:DWORD dst_unused:UNUSED_PAD src0_sel:DWORD src1_sel:WORD_0
	v_cmp_ne_u32_e32 vcc, s22, v148
	s_and_saveexec_b64 s[20:21], vcc
	v_mov_b32_e32 v149, 0x18500
	v_lshl_add_u32 v148, v148, 2, v149
	v_mov_b32_e32 v149, 1
	ds_add_u32 v148, v149
	s_or_b64 exec, exec, s[20:21]
	s_mov_b64 vcc, s[16:17]
	s_waitcnt vmcnt(40)
	v_cndmask_b32_sdwa v147, v147, v160, vcc dst_sel:DWORD dst_unused:UNUSED_PAD src0_sel:DWORD src1_sel:WORD_0
	v_cmp_ne_u32_e32 vcc, s22, v147
	s_and_saveexec_b64 s[16:17], vcc
	v_mov_b32_e32 v148, 0x18500
	v_lshl_add_u32 v147, v147, 2, v148
	v_mov_b32_e32 v148, 1
	ds_add_u32 v147, v148
	s_or_b64 exec, exec, s[16:17]
	s_mov_b64 vcc, s[18:19]
	v_mov_b32_e32 v147, 0xffff
	s_mov_b32 s18, 0xffff
	s_waitcnt vmcnt(39)
	v_cndmask_b32_sdwa v148, v147, v159, vcc dst_sel:DWORD dst_unused:UNUSED_PAD src0_sel:DWORD src1_sel:WORD_0
	v_cmp_ne_u32_e32 vcc, s18, v148
	s_and_saveexec_b64 s[16:17], vcc
	v_mov_b32_e32 v149, 0x18500
	v_lshl_add_u32 v148, v148, 2, v149
	v_mov_b32_e32 v149, 1
	ds_add_u32 v148, v149
	s_or_b64 exec, exec, s[16:17]
	s_mov_b64 vcc, s[12:13]
	s_waitcnt vmcnt(38)
	v_cndmask_b32_sdwa v147, v147, v157, vcc dst_sel:DWORD dst_unused:UNUSED_PAD src0_sel:DWORD src1_sel:WORD_0
	v_cmp_ne_u32_e32 vcc, s18, v147
	s_and_saveexec_b64 s[12:13], vcc
	v_mov_b32_e32 v148, 0x18500
	v_lshl_add_u32 v147, v147, 2, v148
	v_mov_b32_e32 v148, 1
	ds_add_u32 v147, v148
	s_or_b64 exec, exec, s[12:13]
	s_mov_b64 vcc, s[14:15]
	v_mov_b32_e32 v147, 0xffff
	s_mov_b32 s14, 0xffff
	s_waitcnt vmcnt(37)
	v_cndmask_b32_sdwa v148, v147, v156, vcc dst_sel:DWORD dst_unused:UNUSED_PAD src0_sel:DWORD src1_sel:WORD_0
	v_cmp_ne_u32_e32 vcc, s14, v148
	s_and_saveexec_b64 s[12:13], vcc
	v_mov_b32_e32 v149, 0x18500
	v_lshl_add_u32 v148, v148, 2, v149
	v_mov_b32_e32 v149, 1
	ds_add_u32 v148, v149
	s_or_b64 exec, exec, s[12:13]
	s_mov_b64 vcc, s[10:11]
	s_waitcnt vmcnt(36)
	v_cndmask_b32_sdwa v147, v147, v155, vcc dst_sel:DWORD dst_unused:UNUSED_PAD src0_sel:DWORD src1_sel:WORD_0
	v_cmp_ne_u32_e32 vcc, s14, v147
	s_and_saveexec_b64 s[10:11], vcc
	v_mov_b32_e32 v148, 0x18500
	v_lshl_add_u32 v147, v147, 2, v148
	v_mov_b32_e32 v148, 1
	ds_add_u32 v147, v148
	s_or_b64 exec, exec, s[10:11]
	s_mov_b64 vcc, s[4:5]
	v_mov_b32_e32 v147, 0xffff
	s_mov_b32 s10, 0xffff
	s_waitcnt vmcnt(35)
	v_cndmask_b32_sdwa v148, v147, v153, vcc dst_sel:DWORD dst_unused:UNUSED_PAD src0_sel:DWORD src1_sel:WORD_0
	v_cmp_ne_u32_e32 vcc, s10, v148
	s_and_saveexec_b64 s[4:5], vcc
	v_mov_b32_e32 v149, 0x18500
	v_lshl_add_u32 v148, v148, 2, v149
	v_mov_b32_e32 v149, 1
	ds_add_u32 v148, v149
	s_or_b64 exec, exec, s[4:5]
	s_mov_b64 vcc, s[6:7]
	s_waitcnt vmcnt(34)
	v_cndmask_b32_sdwa v147, v147, v154, vcc dst_sel:DWORD dst_unused:UNUSED_PAD src0_sel:DWORD src1_sel:WORD_0
	v_cmp_ne_u32_e32 vcc, s10, v147
	s_and_saveexec_b64 s[4:5], vcc
	v_mov_b32_e32 v148, 0x18500
	v_lshl_add_u32 v147, v147, 2, v148
	v_mov_b32_e32 v148, 1
	ds_add_u32 v147, v148
	s_or_b64 exec, exec, s[4:5]
	s_mov_b64 vcc, s[8:9]
	v_mov_b32_e32 v147, 0xffff
	s_mov_b32 s6, 0xffff
	s_waitcnt vmcnt(33)
	v_cndmask_b32_sdwa v148, v147, v152, vcc dst_sel:DWORD dst_unused:UNUSED_PAD src0_sel:DWORD src1_sel:WORD_0
	v_cmp_ne_u32_e32 vcc, s6, v148
	s_and_saveexec_b64 s[4:5], vcc
	v_mov_b32_e32 v149, 0x18500
	v_lshl_add_u32 v148, v148, 2, v149
	v_mov_b32_e32 v149, 1
	ds_add_u32 v148, v149
	s_or_b64 exec, exec, s[4:5]
	s_mov_b64 vcc, s[0:1]
	s_waitcnt vmcnt(32)
	v_cndmask_b32_sdwa v147, v147, v151, vcc dst_sel:DWORD dst_unused:UNUSED_PAD src0_sel:DWORD src1_sel:WORD_0
	v_cmp_ne_u32_e32 vcc, s6, v147
	s_and_saveexec_b64 s[0:1], vcc
	v_mov_b32_e32 v148, 0x18500
	v_lshl_add_u32 v147, v147, 2, v148
	v_mov_b32_e32 v148, 1
	ds_add_u32 v147, v148
	s_or_b64 exec, exec, s[0:1]
	v_mov_b32_e32 v184, v1
	ds_read2_b32 v[148:149], v169 offset0:220 offset1:225
	ds_read2_b32 v[152:153], v170 offset0:220 offset1:225
	ds_read2_b32 v[154:155], v170 offset0:230 offset1:235
	ds_read2_b32 v[156:157], v169 offset0:230 offset1:235
	v_mov_b32_e32 v161, 0
	s_waitcnt lgkmcnt(3)
	v_add_u32_e32 v147, v148, v1
	s_waitcnt lgkmcnt(2)
	v_cmp_lt_u32_e64 s[20:21], v1, v152
	v_cmp_lt_u32_e32 vcc, v1, v153
	s_waitcnt lgkmcnt(1)
	v_cmp_lt_u32_e64 s[16:17], v1, v154
	v_cndmask_b32_e64 v160, 0, v147, s[20:21]
	v_add_u32_e32 v147, v149, v1
	v_lshl_add_u64 v[162:163], v[160:161], 1, s[26:27]
	v_cndmask_b32_e32 v160, 0, v147, vcc
	s_waitcnt lgkmcnt(0)
	v_add_u32_e32 v147, v156, v1
	v_lshl_add_u64 v[148:149], v[160:161], 1, s[26:27]
	v_cndmask_b32_e64 v160, 0, v147, s[16:17]
	v_add_u32_e32 v147, v157, v1
	ds_read2_b32 v[156:157], v169 offset0:240 offset1:245
	ds_read2_b32 v[172:173], v170 offset0:240 offset1:245
	v_cmp_lt_u32_e64 s[18:19], v1, v155
	v_lshl_add_u64 v[152:153], v[160:161], 1, s[26:27]
	s_waitcnt lgkmcnt(0)
	v_cmp_lt_u32_e64 s[12:13], v1, v172
	v_cndmask_b32_e64 v160, 0, v147, s[18:19]
	v_add_u32_e32 v147, v156, v1
	v_lshl_add_u64 v[154:155], v[160:161], 1, s[26:27]
	v_cndmask_b32_e64 v160, 0, v147, s[12:13]
	v_add_u32_e32 v147, v157, v1
	ds_read2_b32 v[156:157], v169 offset0:250 offset1:255
	ds_read2_b32 v[176:177], v170 offset0:250 offset1:255
	v_cmp_lt_u32_e64 s[14:15], v1, v173
	v_lshl_add_u64 v[174:175], v[160:161], 1, s[26:27]
	s_waitcnt lgkmcnt(0)
	v_cmp_lt_u32_e64 s[10:11], v1, v176
	v_cndmask_b32_e64 v160, 0, v147, s[14:15]
	v_add_u32_e32 v147, v156, v1
	v_lshl_add_u64 v[172:173], v[160:161], 1, s[26:27]
	v_cndmask_b32_e64 v160, 0, v147, s[10:11]
	v_add_u32_e32 v147, v157, v1
	v_cmp_lt_u32_e64 s[4:5], v1, v177
	v_lshl_add_u64 v[178:179], v[160:161], 1, s[26:27]
	s_nop 0
	v_cndmask_b32_e64 v160, 0, v147, s[4:5]
	v_add_u32_e32 v147, 0x400, v169
	ds_read2_b32 v[180:181], v147 offset0:4 offset1:9
	v_add_u32_e32 v147, 0x400, v170
	ds_read2_b32 v[182:183], v147 offset0:4 offset1:9
	v_lshl_add_u64 v[176:177], v[160:161], 1, s[26:27]
	global_load_ushort v159, v[162:163], off
	global_load_ushort v157, v[148:149], off
	global_load_ushort v156, v[152:153], off
	s_nop 0
	global_load_ushort v155, v[154:155], off
	s_nop 0
	global_load_ushort v154, v[174:175], off
	global_load_ushort v153, v[172:173], off
	global_load_ushort v152, v[178:179], off
	global_load_ushort v149, v[176:177], off
	ds_read_b32 v148, v169 offset:1080
	ds_read_b32 v151, v170 offset:1080
	s_waitcnt lgkmcnt(3)
	v_add_u32_e32 v147, v180, v1
	s_waitcnt lgkmcnt(2)
	v_cmp_lt_u32_e64 s[6:7], v1, v182
	v_cmp_lt_u32_e64 s[8:9], v1, v183
	s_waitcnt lgkmcnt(0)
	v_cmp_lt_u32_e64 s[0:1], v1, v151
	v_cndmask_b32_e64 v160, 0, v147, s[6:7]
	v_add_u32_e32 v147, v181, v1
	v_lshl_add_u64 v[162:163], v[160:161], 1, s[26:27]
	v_cndmask_b32_e64 v160, 0, v147, s[8:9]
	v_add_u32_e32 v147, v148, v1
	v_lshl_add_u64 v[172:173], v[160:161], 1, s[26:27]
	v_cndmask_b32_e64 v160, 0, v147, s[0:1]
	v_lshl_add_u64 v[160:161], v[160:161], 1, s[26:27]
	global_load_ushort v151, v[162:163], off
	global_load_ushort v148, v[172:173], off
	global_load_ushort v147, v[160:161], off
	s_waitcnt vmcnt(40)
	v_cvt_pk_bf16_f32 v102, v102, v103
	v_cvt_pk_bf16_f32 v103, v104, v105
	s_waitcnt vmcnt(39)
	v_cvt_pk_bf16_f32 v90, v90, v91
	v_cvt_pk_bf16_f32 v91, v92, v93
	ds_write2_b64 v171, v[102:103], v[90:91] offset0:130 offset1:194
	s_waitcnt vmcnt(28)
	v_cvt_pk_bf16_f32 v90, v126, v127
	v_cvt_pk_bf16_f32 v91, v128, v129
	v_cvt_pk_bf16_f32 v92, v106, v107
	v_cvt_pk_bf16_f32 v93, v108, v109
	v_add_u32_e32 v102, 32, v171
	v_cvt_pk_bf16_f32 v58, v58, v59
	v_cvt_pk_bf16_f32 v59, v60, v61
	v_cvt_pk_bf16_f32 v46, v46, v47
	v_cvt_pk_bf16_f32 v47, v48, v49
	v_add_u32_e32 v48, 0x50, v171
	v_cvt_pk_bf16_f32 v122, v122, v123
	v_cvt_pk_bf16_f32 v123, v124, v125
	v_cvt_pk_bf16_f32 v118, v118, v119
	v_cvt_pk_bf16_f32 v119, v120, v121
	ds_write2st64_b64 v102, v[90:91], v[92:93] offset0:4 offset1:5
	v_cvt_pk_bf16_f32 v78, v78, v79
	v_cvt_pk_bf16_f32 v79, v80, v81
	v_cvt_pk_bf16_f32 v80, v110, v111
	v_cvt_pk_bf16_f32 v81, v112, v113
	v_add_u32_e32 v90, 48, v171
	v_cvt_pk_bf16_f32 v74, v74, v75
	v_cvt_pk_bf16_f32 v75, v76, v77
	v_cvt_pk_bf16_f32 v62, v62, v63
	v_cvt_pk_bf16_f32 v63, v64, v65
	v_add_u32_e32 v64, 64, v171
	ds_write2st64_b64 v48, v[58:59], v[46:47] offset0:10 offset1:11
	v_cvt_pk_bf16_f32 v46, v54, v55
	v_cvt_pk_bf16_f32 v47, v56, v57
	v_cvt_pk_bf16_f32 v30, v30, v31
	v_cvt_pk_bf16_f32 v31, v32, v33
	v_add_u32_e32 v32, 0x60, v171
	v_cvt_pk_bf16_f32 v26, v26, v27
	v_cvt_pk_bf16_f32 v27, v28, v29
	s_waitcnt vmcnt(27)
	v_cvt_pk_bf16_f32 v22, v22, v23
	v_cvt_pk_bf16_f32 v23, v24, v25
	v_add_u32_e32 v24, 0x70, v171
	ds_write2st64_b64 v171, v[122:123], v[118:119] offset1:1
	ds_write2st64_b64 v90, v[78:79], v[80:81] offset0:6 offset1:7
	ds_write2st64_b64 v64, v[74:75], v[62:63] offset0:8 offset1:9
	ds_write2st64_b64 v32, v[46:47], v[30:31] offset0:12 offset1:13
	ds_write2st64_b64 v24, v[26:27], v[22:23] offset0:14 offset1:15
	s_waitcnt vmcnt(26)
	v_cvt_pk_bf16_f32 v22, v138, v139
	v_cvt_pk_bf16_f32 v23, v140, v141
	s_waitcnt vmcnt(25)
	v_cvt_pk_bf16_f32 v24, v134, v135
	v_cvt_pk_bf16_f32 v25, v136, v137
	v_add_u32_e32 v26, 0x80, v171
	ds_write2st64_b64 v26, v[22:23], v[24:25] offset0:16 offset1:17
	s_waitcnt vmcnt(24)
	v_cvt_pk_bf16_f32 v22, v130, v131
	v_cvt_pk_bf16_f32 v23, v132, v133
	s_waitcnt vmcnt(23)
	v_cvt_pk_bf16_f32 v24, v98, v99
	v_cvt_pk_bf16_f32 v25, v100, v101
	v_add_u32_e32 v26, 0x90, v171
	ds_write2st64_b64 v26, v[22:23], v[24:25] offset0:18 offset1:19
	s_waitcnt vmcnt(12)
	v_cvt_pk_bf16_f32 v22, v142, v143
	v_cvt_pk_bf16_f32 v23, v144, v145
	v_cvt_pk_bf16_f32 v24, v114, v115
	v_cvt_pk_bf16_f32 v25, v116, v117
	v_add_u32_e32 v26, 0xa0, v171
	ds_write2st64_b64 v26, v[22:23], v[24:25] offset0:20 offset1:21
	v_cvt_pk_bf16_f32 v22, v86, v87
	v_cvt_pk_bf16_f32 v23, v88, v89
	v_cvt_pk_bf16_f32 v24, v94, v95
	v_cvt_pk_bf16_f32 v25, v96, v97
	v_add_u32_e32 v26, 0xb0, v171
	ds_write2st64_b64 v26, v[22:23], v[24:25] offset0:22 offset1:23
	v_cvt_pk_bf16_f32 v22, v82, v83
	v_cvt_pk_bf16_f32 v23, v84, v85
	v_cvt_pk_bf16_f32 v24, v70, v71
	v_cvt_pk_bf16_f32 v25, v72, v73
	v_add_u32_e32 v26, 0xc0, v171
	ds_write2st64_b64 v26, v[22:23], v[24:25] offset0:24 offset1:25
	v_cvt_pk_bf16_f32 v22, v66, v67
	v_cvt_pk_bf16_f32 v23, v68, v69
	v_cvt_pk_bf16_f32 v24, v42, v43
	v_cvt_pk_bf16_f32 v25, v44, v45
	v_add_u32_e32 v26, 0xd0, v171
	ds_write2st64_b64 v26, v[22:23], v[24:25] offset0:26 offset1:27
	v_cvt_pk_bf16_f32 v22, v50, v51
	v_cvt_pk_bf16_f32 v23, v52, v53
	v_cvt_pk_bf16_f32 v24, v38, v39
	v_cvt_pk_bf16_f32 v25, v40, v41
	v_add_u32_e32 v26, 0xe0, v171
	ds_write2st64_b64 v26, v[22:23], v[24:25] offset0:28 offset1:29
	v_cvt_pk_bf16_f32 v22, v34, v35
	v_cvt_pk_bf16_f32 v23, v36, v37
	s_waitcnt vmcnt(11)
	v_cvt_pk_bf16_f32 v18, v18, v19
	v_cvt_pk_bf16_f32 v19, v20, v21
	v_add_u32_e32 v20, 0xf0, v171
	ds_write2st64_b64 v20, v[22:23], v[18:19] offset0:30 offset1:31
	v_mov_b32_e32 v18, 0x14500
	v_lshl_add_u32 v38, v184, 4, v18
	ds_read_b128 v[18:21], v38
	ds_read_b128 v[22:25], v38 offset:1024
	ds_read_b128 v[26:29], v168
	ds_read_b128 v[30:33], v168 offset:16
	s_waitcnt lgkmcnt(1)
	v_mfma_f32_16x16x32_bf16 v[18:21], v[18:21], v[26:29], 0
	ds_read_b128 v[26:29], v38 offset:2048
	ds_read_b128 v[34:37], v38 offset:3072
	s_waitcnt lgkmcnt(2)
	v_mfma_f32_16x16x32_bf16 v[18:21], v[22:25], v[30:33], v[18:21]
	ds_read_b128 v[22:25], v168 offset:32
	ds_read_b128 v[30:33], v168 offset:48
	s_waitcnt lgkmcnt(1)
	v_mfma_f32_16x16x32_bf16 v[18:21], v[26:29], v[22:25], v[18:21]
	s_waitcnt lgkmcnt(0)
	v_mfma_f32_16x16x32_bf16 v[18:21], v[34:37], v[30:33], v[18:21]
	ds_read_b128 v[22:25], v38 offset:4096
	ds_read_b128 v[26:29], v38 offset:5120
	ds_read_b128 v[30:33], v168 offset:64
	ds_read_b128 v[34:37], v168 offset:80
	s_waitcnt lgkmcnt(1)
	v_mfma_f32_16x16x32_bf16 v[18:21], v[22:25], v[30:33], v[18:21]
	ds_read_b128 v[22:25], v38 offset:6144
	ds_read_b128 v[30:33], v38 offset:7168
	s_waitcnt lgkmcnt(2)
	v_mfma_f32_16x16x32_bf16 v[18:21], v[26:29], v[34:37], v[18:21]
	ds_read_b128 v[26:29], v168 offset:96
	ds_read_b128 v[34:37], v168 offset:112
	s_waitcnt lgkmcnt(1)
	v_mfma_f32_16x16x32_bf16 v[18:21], v[22:25], v[26:29], v[18:21]
	s_waitcnt lgkmcnt(0)
	v_mfma_f32_16x16x32_bf16 v[18:21], v[30:33], v[34:37], v[18:21]
	ds_read_b128 v[22:25], v38 offset:8192
	ds_read_b128 v[26:29], v38 offset:9216
	ds_read_b128 v[30:33], v168 offset:128
	ds_read_b128 v[34:37], v168 offset:144
	s_waitcnt lgkmcnt(1)
	v_mfma_f32_16x16x32_bf16 v[18:21], v[22:25], v[30:33], v[18:21]
	ds_read_b128 v[22:25], v38 offset:10240
	ds_read_b128 v[30:33], v38 offset:11264
	s_waitcnt lgkmcnt(2)
	v_mfma_f32_16x16x32_bf16 v[18:21], v[26:29], v[34:37], v[18:21]
	ds_read_b128 v[26:29], v168 offset:160
	ds_read_b128 v[34:37], v168 offset:176
	s_waitcnt lgkmcnt(1)
	v_mfma_f32_16x16x32_bf16 v[18:21], v[22:25], v[26:29], v[18:21]
	s_waitcnt lgkmcnt(0)
	v_mfma_f32_16x16x32_bf16 v[18:21], v[30:33], v[34:37], v[18:21]
	ds_read_b128 v[22:25], v38 offset:12288
	ds_read_b128 v[26:29], v38 offset:13312
	ds_read_b128 v[30:33], v168 offset:192
	ds_read_b128 v[34:37], v168 offset:208
	s_waitcnt lgkmcnt(1)
	v_mfma_f32_16x16x32_bf16 v[18:21], v[22:25], v[30:33], v[18:21]
	ds_read_b128 v[22:25], v38 offset:14336
	ds_read_b128 v[30:33], v38 offset:15360
	s_waitcnt lgkmcnt(2)
	v_mfma_f32_16x16x32_bf16 v[18:21], v[26:29], v[34:37], v[18:21]
	ds_read_b128 v[26:29], v168 offset:224
	ds_read_b128 v[34:37], v168 offset:240
	s_waitcnt lgkmcnt(1)
	v_mfma_f32_16x16x32_bf16 v[18:21], v[22:25], v[26:29], v[18:21]
	s_waitcnt lgkmcnt(0)
	v_mfma_f32_16x16x32_bf16 v[18:21], v[30:33], v[34:37], v[18:21]
	s_waitcnt vmcnt(10)
	v_cmp_ne_u16_e64 s[22:23], -1, v159
	s_and_b64 s[22:23], s[20:21], s[22:23]
	s_and_saveexec_b64 s[20:21], s[22:23]
	v_and_b32_e32 v22, 0xffff, v159
	v_mov_b32_e32 v23, 0x18500
	v_lshl_add_u32 v22, v22, 2, v23
	v_mov_b32_e32 v23, 1
	ds_add_u32 v22, v23
	s_or_b64 exec, exec, s[20:21]
	v_mov_b32_e32 v22, 0xffff
	s_mov_b32 s22, 0xffff
	s_waitcnt vmcnt(9)
	v_cndmask_b32_sdwa v23, v22, v157, vcc dst_sel:DWORD dst_unused:UNUSED_PAD src0_sel:DWORD src1_sel:WORD_0
	v_cmp_ne_u32_e32 vcc, s22, v23
	s_and_saveexec_b64 s[20:21], vcc
	v_mov_b32_e32 v24, 0x18500
	v_lshl_add_u32 v23, v23, 2, v24
	v_mov_b32_e32 v24, 1
	ds_add_u32 v23, v24
	s_or_b64 exec, exec, s[20:21]
	s_mov_b64 vcc, s[16:17]
	s_waitcnt vmcnt(8)
	v_cndmask_b32_sdwa v22, v22, v156, vcc dst_sel:DWORD dst_unused:UNUSED_PAD src0_sel:DWORD src1_sel:WORD_0
	v_cmp_ne_u32_e32 vcc, s22, v22
	s_and_saveexec_b64 s[16:17], vcc
	v_mov_b32_e32 v23, 0x18500
	v_lshl_add_u32 v22, v22, 2, v23
	v_mov_b32_e32 v23, 1
	ds_add_u32 v22, v23
	s_or_b64 exec, exec, s[16:17]
	s_mov_b64 vcc, s[18:19]
	v_mov_b32_e32 v22, 0xffff
	s_mov_b32 s18, 0xffff
	s_waitcnt vmcnt(7)
	v_cndmask_b32_sdwa v23, v22, v155, vcc dst_sel:DWORD dst_unused:UNUSED_PAD src0_sel:DWORD src1_sel:WORD_0
	v_cmp_ne_u32_e32 vcc, s18, v23
	s_and_saveexec_b64 s[16:17], vcc
	v_mov_b32_e32 v24, 0x18500
	v_lshl_add_u32 v23, v23, 2, v24
	v_mov_b32_e32 v24, 1
	ds_add_u32 v23, v24
	s_or_b64 exec, exec, s[16:17]
	s_mov_b64 vcc, s[12:13]
	s_waitcnt vmcnt(6)
	v_cndmask_b32_sdwa v22, v22, v154, vcc dst_sel:DWORD dst_unused:UNUSED_PAD src0_sel:DWORD src1_sel:WORD_0
	v_cmp_ne_u32_e32 vcc, s18, v22
	s_and_saveexec_b64 s[12:13], vcc
	v_mov_b32_e32 v23, 0x18500
	v_lshl_add_u32 v22, v22, 2, v23
	v_mov_b32_e32 v23, 1
	ds_add_u32 v22, v23
	s_or_b64 exec, exec, s[12:13]
	s_mov_b64 vcc, s[14:15]
	v_mov_b32_e32 v22, 0xffff
	s_mov_b32 s14, 0xffff
	s_waitcnt vmcnt(5)
	v_cndmask_b32_sdwa v23, v22, v153, vcc dst_sel:DWORD dst_unused:UNUSED_PAD src0_sel:DWORD src1_sel:WORD_0
	v_cmp_ne_u32_e32 vcc, s14, v23
	s_and_saveexec_b64 s[12:13], vcc
	v_mov_b32_e32 v24, 0x18500
	v_lshl_add_u32 v23, v23, 2, v24
	v_mov_b32_e32 v24, 1
	ds_add_u32 v23, v24
	s_or_b64 exec, exec, s[12:13]
	s_mov_b64 vcc, s[10:11]
	s_waitcnt vmcnt(4)
	v_cndmask_b32_sdwa v22, v22, v152, vcc dst_sel:DWORD dst_unused:UNUSED_PAD src0_sel:DWORD src1_sel:WORD_0
	v_cmp_ne_u32_e32 vcc, s14, v22
	s_and_saveexec_b64 s[10:11], vcc
	v_mov_b32_e32 v23, 0x18500
	v_lshl_add_u32 v22, v22, 2, v23
	v_mov_b32_e32 v23, 1
	ds_add_u32 v22, v23
	s_or_b64 exec, exec, s[10:11]
	s_mov_b64 vcc, s[4:5]
	v_mov_b32_e32 v22, 0xffff
	s_mov_b32 s10, 0xffff
	s_waitcnt vmcnt(3)
	v_cndmask_b32_sdwa v23, v22, v149, vcc dst_sel:DWORD dst_unused:UNUSED_PAD src0_sel:DWORD src1_sel:WORD_0
	v_cmp_ne_u32_e32 vcc, s10, v23
	s_and_saveexec_b64 s[4:5], vcc
	v_mov_b32_e32 v24, 0x18500
	v_lshl_add_u32 v23, v23, 2, v24
	v_mov_b32_e32 v24, 1
	ds_add_u32 v23, v24
	s_or_b64 exec, exec, s[4:5]
	s_mov_b64 vcc, s[6:7]
	s_waitcnt vmcnt(2)
	v_cndmask_b32_sdwa v22, v22, v151, vcc dst_sel:DWORD dst_unused:UNUSED_PAD src0_sel:DWORD src1_sel:WORD_0
	v_cmp_ne_u32_e32 vcc, s10, v22
	s_and_saveexec_b64 s[4:5], vcc
	v_mov_b32_e32 v23, 0x18500
	v_lshl_add_u32 v22, v22, 2, v23
	v_mov_b32_e32 v23, 1
	ds_add_u32 v22, v23
	s_or_b64 exec, exec, s[4:5]
	s_mov_b64 vcc, s[8:9]
	v_mov_b32_e32 v22, 0xffff
	s_mov_b32 s6, 0xffff
	s_waitcnt vmcnt(1)
	v_cndmask_b32_sdwa v23, v22, v148, vcc dst_sel:DWORD dst_unused:UNUSED_PAD src0_sel:DWORD src1_sel:WORD_0
	v_cmp_ne_u32_e32 vcc, s6, v23
	s_and_saveexec_b64 s[4:5], vcc
	v_mov_b32_e32 v24, 0x18500
	v_lshl_add_u32 v23, v23, 2, v24
	v_mov_b32_e32 v24, 1
	ds_add_u32 v23, v24
	s_or_b64 exec, exec, s[4:5]
	s_mov_b64 vcc, s[0:1]
	s_waitcnt vmcnt(0)
	v_cndmask_b32_sdwa v22, v22, v147, vcc dst_sel:DWORD dst_unused:UNUSED_PAD src0_sel:DWORD src1_sel:WORD_0
	v_cmp_ne_u32_e32 vcc, s6, v22
	s_and_saveexec_b64 s[0:1], vcc
	v_mov_b32_e32 v23, 0x18500
	v_lshl_add_u32 v22, v22, 2, v23
	v_mov_b32_e32 v23, 1
	ds_add_u32 v22, v23
	s_or_b64 exec, exec, s[0:1]
	s_waitcnt vmcnt(0)
	v_mov_b32_e32 v35, 1
	s_mov_b64 exec, s[46:47]
	v_lshlrev_b32_e32 v34, 2, v192
	v_add_u32_e32 v34, 0x18500, v34
	ds_add_u32 v34, v35
	s_mov_b64 exec, s[48:49]
	v_lshlrev_b32_e32 v34, 2, v193
	v_add_u32_e32 v34, 0x18500, v34
	ds_add_u32 v34, v35
	s_mov_b64 exec, s[50:51]
	v_lshlrev_b32_e32 v34, 2, v194
	v_add_u32_e32 v34, 0x18500, v34
	ds_add_u32 v34, v35
	s_mov_b64 exec, s[52:53]
	v_lshlrev_b32_e32 v34, 2, v195
	v_add_u32_e32 v34, 0x18500, v34
	ds_add_u32 v34, v35
	s_mov_b64 exec, -1
.Lk2t_loop:
	s_cmp_eq_u64 s[42:43], 0
	s_cbranch_scc1 .Lk2t_done
	s_mov_b64 s[46:47], 0
	s_mov_b64 s[48:49], 0
	s_mov_b64 s[50:51], 0
	s_mov_b64 s[52:53], 0
	s_ff1_i32_b64 s44, s[42:43]
	v_readlane_b32 s45, v196, s44
	v_readlane_b32 s54, v197, s44
	s_bitset0_b64 s[42:43], s44
	s_nop 0
	v_cmp_gt_u32_e64 s[46:47], s45, v198
	s_add_i32 s54, s54, 64
	s_lshl_b32 s54, s54, 1
	s_add_u32 s56, s26, s54
	s_addc_u32 s57, s27, 0
	s_mov_b64 exec, s[46:47]
	global_load_ushort v30, v199, s[56:57]
	s_mov_b64 exec, -1
	s_cmp_eq_u64 s[42:43], 0
	s_cbranch_scc1 .Lk2t_proc
	s_ff1_i32_b64 s44, s[42:43]
	v_readlane_b32 s45, v196, s44
	v_readlane_b32 s54, v197, s44
	s_bitset0_b64 s[42:43], s44
	s_nop 0
	v_cmp_gt_u32_e64 s[48:49], s45, v198
	s_add_i32 s54, s54, 64
	s_lshl_b32 s54, s54, 1
	s_add_u32 s58, s26, s54
	s_addc_u32 s59, s27, 0
	s_mov_b64 exec, s[48:49]
	global_load_ushort v31, v199, s[58:59]
	s_mov_b64 exec, -1
	s_cmp_eq_u64 s[42:43], 0
	s_cbranch_scc1 .Lk2t_proc
	s_ff1_i32_b64 s44, s[42:43]
	v_readlane_b32 s45, v196, s44
	v_readlane_b32 s54, v197, s44
	s_bitset0_b64 s[42:43], s44
	s_nop 0
	v_cmp_gt_u32_e64 s[50:51], s45, v198
	s_add_i32 s54, s54, 64
	s_lshl_b32 s54, s54, 1
	s_add_u32 s60, s26, s54
	s_addc_u32 s61, s27, 0
	s_mov_b64 exec, s[50:51]
	global_load_ushort v32, v199, s[60:61]
	s_mov_b64 exec, -1
	s_cmp_eq_u64 s[42:43], 0
	s_cbranch_scc1 .Lk2t_proc
	s_ff1_i32_b64 s44, s[42:43]
	v_readlane_b32 s45, v196, s44
	v_readlane_b32 s54, v197, s44
	s_bitset0_b64 s[42:43], s44
	s_nop 0
	v_cmp_gt_u32_e64 s[52:53], s45, v198
	s_add_i32 s54, s54, 64
	s_lshl_b32 s54, s54, 1
	s_add_u32 s62, s26, s54
	s_addc_u32 s63, s27, 0
	s_mov_b64 exec, s[52:53]
	global_load_ushort v33, v199, s[62:63]
	s_mov_b64 exec, -1
.Lk2t_proc:
	s_waitcnt vmcnt(0)
	s_mov_b64 exec, s[46:47]
	v_lshlrev_b32_e32 v34, 2, v30
	v_add_u32_e32 v34, 0x18500, v34
	ds_add_u32 v34, v35
	s_mov_b64 exec, s[48:49]
	v_lshlrev_b32_e32 v34, 2, v31
	v_add_u32_e32 v34, 0x18500, v34
	ds_add_u32 v34, v35
	s_mov_b64 exec, s[50:51]
	v_lshlrev_b32_e32 v34, 2, v32
	v_add_u32_e32 v34, 0x18500, v34
	ds_add_u32 v34, v35
	s_mov_b64 exec, s[52:53]
	v_lshlrev_b32_e32 v34, 2, v33
	v_add_u32_e32 v34, 0x18500, v34
	ds_add_u32 v34, v35
	s_mov_b64 exec, -1
	s_branch .Lk2t_loop

	.amdhsa_kernel _Z6k_gemmPKfS0_PKtPKjPfPt
		.amdhsa_group_segment_fixed_size 103492
		.amdhsa_private_segment_fixed_size 0
		.amdhsa_kernarg_size 48
		.amdhsa_user_sgpr_count 2
		.amdhsa_user_sgpr_dispatch_ptr 0
		.amdhsa_user_sgpr_queue_ptr 0
		.amdhsa_user_sgpr_kernarg_segment_ptr 1
		.amdhsa_user_sgpr_dispatch_id 0
		.amdhsa_user_sgpr_kernarg_preload_length 0
		.amdhsa_user_sgpr_kernarg_preload_offset 0
		.amdhsa_user_sgpr_private_segment_size 0
		.amdhsa_uses_dynamic_stack 0
		.amdhsa_enable_private_segment 0
		.amdhsa_system_sgpr_workgroup_id_x 1
		.amdhsa_system_sgpr_workgroup_id_y 0
		.amdhsa_system_sgpr_workgroup_id_z 0
		.amdhsa_system_sgpr_workgroup_info 0
		.amdhsa_system_vgpr_workitem_id 0
		.amdhsa_next_free_vgpr 200
		.amdhsa_next_free_sgpr 96
		.amdhsa_accum_offset 200
		.amdhsa_reserve_vcc 1
		.amdhsa_float_round_mode_32 0
		.amdhsa_float_round_mode_16_64 0
		.amdhsa_float_denorm_mode_32 3
		.amdhsa_float_denorm_mode_16_64 3
		.amdhsa_dx10_clamp 1
		.amdhsa_ieee_mode 1
		.amdhsa_fp16_overflow 0
		.amdhsa_tg_split 0
		.amdhsa_exception_fp_ieee_invalid_op 0
		.amdhsa_exception_fp_denorm_src 0
		.amdhsa_exception_fp_ieee_div_zero 0
		.amdhsa_exception_fp_ieee_overflow 0
		.amdhsa_exception_fp_ieee_underflow 0
		.amdhsa_exception_fp_ieee_inexact 0
		.amdhsa_exception_int_div_zero 0
	.end_amdhsa_kernel

amdhsa.kernels:
  - .agpr_count:     0
    .args:
      - .actual_access:  read_only
        .address_space:  global
        .offset:         0
        .size:           8
        .value_kind:     global_buffer
      - .actual_access:  read_only
        .address_space:  global
        .offset:         8
        .size:           8
        .value_kind:     global_buffer
      - .actual_access:  write_only
        .address_space:  global
        .offset:         16
        .size:           8
        .value_kind:     global_buffer
      - .actual_access:  write_only
        .address_space:  global
        .offset:         24
        .size:           8
        .value_kind:     global_buffer
      - .actual_access:  write_only
        .address_space:  global
        .offset:         32
        .size:           8
        .value_kind:     global_buffer
      - .actual_access:  write_only
        .address_space:  global
        .offset:         40
        .size:           8
        .value_kind:     global_buffer
      - .actual_access:  write_only
        .address_space:  global
        .offset:         48
        .size:           8
        .value_kind:     global_buffer
    .group_segment_fixed_size: 107840
    .kernarg_segment_align: 8
    .kernarg_segment_size: 56
    .language:       OpenCL C
    .language_version:
      - 2
      - 0
    .max_flat_workgroup_size: 1024
    .name:           _Z6k_partPKiS0_PjPtS1_S1_S1_
    .private_segment_fixed_size: 0
    .sgpr_count:     50
    .sgpr_spill_count: 0
    .symbol:         _Z6k_partPKiS0_PjPtS1_S1_S1_.kd
    .uniform_work_group_size: 1
    .uses_dynamic_stack: false
    .vgpr_count:     123
    .vgpr_spill_count: 0
    .wavefront_size: 64
  - .agpr_count:     0
    .args:
      - .actual_access:  read_only
        .address_space:  global
        .offset:         0
        .size:           8
        .value_kind:     global_buffer
      - .actual_access:  read_only
        .address_space:  global
        .offset:         8
        .size:           8
        .value_kind:     global_buffer
      - .actual_access:  read_only
        .address_space:  global
        .offset:         16
        .size:           8
        .value_kind:     global_buffer
      - .actual_access:  read_only
        .address_space:  global
        .offset:         24
        .size:           8
        .value_kind:     global_buffer
      - .actual_access:  write_only
        .address_space:  global
        .offset:         32
        .size:           8
        .value_kind:     global_buffer
      - .actual_access:  write_only
        .address_space:  global
        .offset:         40
        .size:           8
        .value_kind:     global_buffer
    .group_segment_fixed_size: 103492
    .kernarg_segment_align: 8
    .kernarg_segment_size: 48
    .language:       OpenCL C
    .language_version:
      - 2
      - 0
    .max_flat_workgroup_size: 320
    .name:           _Z6k_gemmPKfS0_PKtPKjPfPt
    .private_segment_fixed_size: 0
    .sgpr_count:     43
    .sgpr_spill_count: 0
    .symbol:         _Z6k_gemmPKfS0_PKtPKjPfPt.kd
    .uniform_work_group_size: 1
    .uses_dynamic_stack: false
    .vgpr_count:     200
    .vgpr_spill_count: 0
    .wavefront_size: 64
  - .agpr_count:     0
    .args:
      - .actual_access:  read_only
        .address_space:  global
        .offset:         0
        .size:           8
        .value_kind:     global_buffer
      - .actual_access:  read_only
        .address_space:  global
        .offset:         8
        .size:           8
        .value_kind:     global_buffer
      - .actual_access:  read_only
        .address_space:  global
        .offset:         16
        .size:           8
        .value_kind:     global_buffer
      - .actual_access:  read_only
        .address_space:  global
        .offset:         24
        .size:           8
        .value_kind:     global_buffer
      - .actual_access:  read_only
        .address_space:  global
        .offset:         32
        .size:           8
        .value_kind:     global_buffer
      - .address_space:  global
        .offset:         40
        .size:           8
        .value_kind:     global_buffer
      - .actual_access:  read_only
        .address_space:  global
        .offset:         48
        .size:           8
        .value_kind:     global_buffer
      - .actual_access:  read_only
        .address_space:  global
        .offset:         56
        .size:           8
        .value_kind:     global_buffer
      - .actual_access:  write_only
        .address_space:  global
        .offset:         64
        .size:           8
        .value_kind:     global_buffer
      - .address_space:  global
        .offset:         72
        .size:           8
        .value_kind:     global_buffer
      - .offset:         80
        .size:           4
        .value_kind:     hidden_block_count_x
      - .offset:         84
        .size:           4
        .value_kind:     hidden_block_count_y
      - .offset:         88
        .size:           4
        .value_kind:     hidden_block_count_z
      - .offset:         92
        .size:           2
        .value_kind:     hidden_group_size_x
      - .offset:         94
        .size:           2
        .value_kind:     hidden_group_size_y
      - .offset:         96
        .size:           2
        .value_kind:     hidden_group_size_z
      - .offset:         98
        .size:           2
        .value_kind:     hidden_remainder_x
      - .offset:         100
        .size:           2
        .value_kind:     hidden_remainder_y
      - .offset:         102
        .size:           2
        .value_kind:     hidden_remainder_z
      - .offset:         120
        .size:           8
        .value_kind:     hidden_global_offset_x
      - .offset:         128
        .size:           8
        .value_kind:     hidden_global_offset_y
      - .offset:         136
        .size:           8
        .value_kind:     hidden_global_offset_z
      - .offset:         144
        .size:           2
        .value_kind:     hidden_grid_dims
    .group_segment_fixed_size: 138560
    .kernarg_segment_align: 8
    .kernarg_segment_size: 336
    .language:       OpenCL C
    .language_version:
      - 2
      - 0
    .max_flat_workgroup_size: 1024
    .name:           _Z6k_aggfPKjS0_PKtPKfS4_PtS4_S4_PfPj
    .private_segment_fixed_size: 0
    .sgpr_count:     81
    .sgpr_spill_count: 0
    .symbol:         _Z6k_aggfPKjS0_PKtPKfS4_PtS4_S4_PfPj.kd
    .uniform_work_group_size: 1
    .uses_dynamic_stack: false
    .vgpr_count:     128
    .vgpr_spill_count: 0
    .wavefront_size: 64
